# gelu tanh: branchless 1-2/(1+exp2(2|y|log2e)) f32 (abs err ~1e-7) replaces hipcc tanhf two-path expansion in sgu and sgu_prep
# speedup vs baseline: 1.0174x; 1.0091x over previous
.LBB0_379:
	s_andn2_saveexec_b64 s[46:47], s[46:47]
	s_cbranch_execz .LBB0_413
	v_add_f32_e64 v120, |v126|, |v126|
	v_mul_f32_e32 v120, 0x3fb8aa3b, v120
	v_exp_f32_e32 v120, v120
	s_nop 0
	v_add_f32_e32 v120, 1.0, v120
	v_rcp_f32_e32 v120, v120
	s_nop 0
	v_fma_f32 v120, v120, -2.0, 1.0
	v_add_f32_e64 v121, |v127|, |v127|
	v_mul_f32_e32 v121, 0x3fb8aa3b, v121
	v_exp_f32_e32 v121, v121
	s_nop 0
	v_add_f32_e32 v121, 1.0, v121
	v_rcp_f32_e32 v121, v121
	s_nop 0
	v_fma_f32 v121, v121, -2.0, 1.0
	v_add_f32_e64 v122, |v114|, |v114|
	v_mul_f32_e32 v122, 0x3fb8aa3b, v122
	v_exp_f32_e32 v122, v122
	s_nop 0
	v_add_f32_e32 v122, 1.0, v122
	v_rcp_f32_e32 v122, v122
	s_nop 0
	v_fma_f32 v122, v122, -2.0, 1.0
	v_add_f32_e64 v123, |v115|, |v115|
	v_mul_f32_e32 v123, 0x3fb8aa3b, v123
	v_exp_f32_e32 v123, v123
	s_nop 0
	v_add_f32_e32 v123, 1.0, v123
	v_rcp_f32_e32 v123, v123
	s_nop 0
	v_fma_f32 v123, v123, -2.0, 1.0
	v_add_f32_e64 v124, |v118|, |v118|
	v_mul_f32_e32 v124, 0x3fb8aa3b, v124
	v_exp_f32_e32 v124, v124
	s_nop 0
	v_add_f32_e32 v124, 1.0, v124
	v_rcp_f32_e32 v124, v124
	s_nop 0
	v_fma_f32 v124, v124, -2.0, 1.0
	v_add_f32_e64 v125, |v119|, |v119|
	v_mul_f32_e32 v125, 0x3fb8aa3b, v125
	v_exp_f32_e32 v125, v125
	s_nop 0
	v_add_f32_e32 v125, 1.0, v125
	v_rcp_f32_e32 v125, v125
	s_nop 0
	v_fma_f32 v125, v125, -2.0, 1.0
	v_add_f32_e64 v128, |v116|, |v116|
	v_mul_f32_e32 v128, 0x3fb8aa3b, v128
	v_exp_f32_e32 v128, v128
	s_nop 0
	v_add_f32_e32 v128, 1.0, v128
	v_rcp_f32_e32 v128, v128
	s_nop 0
	v_fma_f32 v128, v128, -2.0, 1.0
	v_add_f32_e64 v129, |v117|, |v117|
	v_mul_f32_e32 v129, 0x3fb8aa3b, v129
	v_exp_f32_e32 v129, v129
	s_nop 0
	v_add_f32_e32 v129, 1.0, v129
	v_rcp_f32_e32 v129, v129
	s_nop 0
	v_fma_f32 v129, v129, -2.0, 1.0
	v_bfi_b32 v126, s85, v120, v126
	v_bfi_b32 v127, s85, v121, v127
	v_bfi_b32 v114, s85, v122, v114
	v_bfi_b32 v115, s85, v123, v115
	v_bfi_b32 v118, s85, v124, v118
	v_bfi_b32 v119, s85, v125, v119
	v_bfi_b32 v116, s85, v128, v116
	v_bfi_b32 v117, s85, v129, v117

.LBB0_436:
	s_andn2_saveexec_b64 s[46:47], s[46:47]
	s_cbranch_execz .LBB0_470
	v_add_f32_e64 v118, |v114|, |v114|
	v_mul_f32_e32 v118, 0x3fb8aa3b, v118
	v_exp_f32_e32 v118, v118
	s_nop 0
	v_add_f32_e32 v118, 1.0, v118
	v_rcp_f32_e32 v118, v118
	s_nop 0
	v_fma_f32 v118, v118, -2.0, 1.0
	v_add_f32_e64 v119, |v115|, |v115|
	v_mul_f32_e32 v119, 0x3fb8aa3b, v119
	v_exp_f32_e32 v119, v119
	s_nop 0
	v_add_f32_e32 v119, 1.0, v119
	v_rcp_f32_e32 v119, v119
	s_nop 0
	v_fma_f32 v119, v119, -2.0, 1.0
	v_add_f32_e64 v122, |v110|, |v110|
	v_mul_f32_e32 v122, 0x3fb8aa3b, v122
	v_exp_f32_e32 v122, v122
	s_nop 0
	v_add_f32_e32 v122, 1.0, v122
	v_rcp_f32_e32 v122, v122
	s_nop 0
	v_fma_f32 v122, v122, -2.0, 1.0
	v_add_f32_e64 v123, |v111|, |v111|
	v_mul_f32_e32 v123, 0x3fb8aa3b, v123
	v_exp_f32_e32 v123, v123
	s_nop 0
	v_add_f32_e32 v123, 1.0, v123
	v_rcp_f32_e32 v123, v123
	s_nop 0
	v_fma_f32 v123, v123, -2.0, 1.0
	v_add_f32_e64 v124, |v116|, |v116|
	v_mul_f32_e32 v124, 0x3fb8aa3b, v124
	v_exp_f32_e32 v124, v124
	s_nop 0
	v_add_f32_e32 v124, 1.0, v124
	v_rcp_f32_e32 v124, v124
	s_nop 0
	v_fma_f32 v124, v124, -2.0, 1.0
	v_add_f32_e64 v125, |v117|, |v117|
	v_mul_f32_e32 v125, 0x3fb8aa3b, v125
	v_exp_f32_e32 v125, v125
	s_nop 0
	v_add_f32_e32 v125, 1.0, v125
	v_rcp_f32_e32 v125, v125
	s_nop 0
	v_fma_f32 v125, v125, -2.0, 1.0
	v_add_f32_e64 v126, |v112|, |v112|
	v_mul_f32_e32 v126, 0x3fb8aa3b, v126
	v_exp_f32_e32 v126, v126
	s_nop 0
	v_add_f32_e32 v126, 1.0, v126
	v_rcp_f32_e32 v126, v126
	s_nop 0
	v_fma_f32 v126, v126, -2.0, 1.0
	v_add_f32_e64 v127, |v113|, |v113|
	v_mul_f32_e32 v127, 0x3fb8aa3b, v127
	v_exp_f32_e32 v127, v127
	s_nop 0
	v_add_f32_e32 v127, 1.0, v127
	v_rcp_f32_e32 v127, v127
	s_nop 0
	v_fma_f32 v127, v127, -2.0, 1.0
	v_bfi_b32 v114, s85, v118, v114
	v_bfi_b32 v115, s85, v119, v115
	v_bfi_b32 v110, s85, v122, v110
	v_bfi_b32 v111, s85, v123, v111
	v_bfi_b32 v116, s85, v124, v116
	v_bfi_b32 v117, s85, v125, v117
	v_bfi_b32 v112, s85, v126, v112
	v_bfi_b32 v113, s85, v127, v113

.LBB0_487:
	s_andn2_saveexec_b64 s[44:45], s[44:45]
	s_cbranch_execz .LBB0_521
	v_add_f32_e64 v114, |v110|, |v110|
	v_mul_f32_e32 v114, 0x3fb8aa3b, v114
	v_exp_f32_e32 v114, v114
	s_nop 0
	v_add_f32_e32 v114, 1.0, v114
	v_rcp_f32_e32 v114, v114
	s_nop 0
	v_fma_f32 v114, v114, -2.0, 1.0
	v_add_f32_e64 v115, |v111|, |v111|
	v_mul_f32_e32 v115, 0x3fb8aa3b, v115
	v_exp_f32_e32 v115, v115
	s_nop 0
	v_add_f32_e32 v115, 1.0, v115
	v_rcp_f32_e32 v115, v115
	s_nop 0
	v_fma_f32 v115, v115, -2.0, 1.0
	v_add_f32_e64 v117, |v106|, |v106|
	v_mul_f32_e32 v117, 0x3fb8aa3b, v117
	v_exp_f32_e32 v117, v117
	s_nop 0
	v_add_f32_e32 v117, 1.0, v117
	v_rcp_f32_e32 v117, v117
	s_nop 0
	v_fma_f32 v117, v117, -2.0, 1.0
	v_add_f32_e64 v118, |v107|, |v107|
	v_mul_f32_e32 v118, 0x3fb8aa3b, v118
	v_exp_f32_e32 v118, v118
	s_nop 0
	v_add_f32_e32 v118, 1.0, v118
	v_rcp_f32_e32 v118, v118
	s_nop 0
	v_fma_f32 v118, v118, -2.0, 1.0
	v_add_f32_e64 v119, |v112|, |v112|
	v_mul_f32_e32 v119, 0x3fb8aa3b, v119
	v_exp_f32_e32 v119, v119
	s_nop 0
	v_add_f32_e32 v119, 1.0, v119
	v_rcp_f32_e32 v119, v119
	s_nop 0
	v_fma_f32 v119, v119, -2.0, 1.0
	v_add_f32_e64 v121, |v113|, |v113|
	v_mul_f32_e32 v121, 0x3fb8aa3b, v121
	v_exp_f32_e32 v121, v121
	s_nop 0
	v_add_f32_e32 v121, 1.0, v121
	v_rcp_f32_e32 v121, v121
	s_nop 0
	v_fma_f32 v121, v121, -2.0, 1.0
	v_add_f32_e64 v122, |v108|, |v108|
	v_mul_f32_e32 v122, 0x3fb8aa3b, v122
	v_exp_f32_e32 v122, v122
	s_nop 0
	v_add_f32_e32 v122, 1.0, v122
	v_rcp_f32_e32 v122, v122
	s_nop 0
	v_fma_f32 v122, v122, -2.0, 1.0
	v_add_f32_e64 v123, |v109|, |v109|
	v_mul_f32_e32 v123, 0x3fb8aa3b, v123
	v_exp_f32_e32 v123, v123
	s_nop 0
	v_add_f32_e32 v123, 1.0, v123
	v_rcp_f32_e32 v123, v123
	s_nop 0
	v_fma_f32 v123, v123, -2.0, 1.0
	v_bfi_b32 v110, s85, v114, v110
	v_bfi_b32 v111, s85, v115, v111
	v_bfi_b32 v106, s85, v117, v106
	v_bfi_b32 v107, s85, v118, v107
	v_bfi_b32 v112, s85, v119, v112
	v_bfi_b32 v113, s85, v121, v113
	v_bfi_b32 v108, s85, v122, v108
	v_bfi_b32 v109, s85, v123, v109

.LBB0_538:
	s_andn2_saveexec_b64 s[42:43], s[42:43]
	s_cbranch_execz .LBB0_572
	v_add_f32_e64 v110, |v106|, |v106|
	v_mul_f32_e32 v110, 0x3fb8aa3b, v110
	v_exp_f32_e32 v110, v110
	s_nop 0
	v_add_f32_e32 v110, 1.0, v110
	v_rcp_f32_e32 v110, v110
	s_nop 0
	v_fma_f32 v110, v110, -2.0, 1.0
	v_add_f32_e64 v111, |v107|, |v107|
	v_mul_f32_e32 v111, 0x3fb8aa3b, v111
	v_exp_f32_e32 v111, v111
	s_nop 0
	v_add_f32_e32 v111, 1.0, v111
	v_rcp_f32_e32 v111, v111
	s_nop 0
	v_fma_f32 v111, v111, -2.0, 1.0
	v_add_f32_e64 v113, |v102|, |v102|
	v_mul_f32_e32 v113, 0x3fb8aa3b, v113
	v_exp_f32_e32 v113, v113
	s_nop 0
	v_add_f32_e32 v113, 1.0, v113
	v_rcp_f32_e32 v113, v113
	s_nop 0
	v_fma_f32 v113, v113, -2.0, 1.0
	v_add_f32_e64 v114, |v103|, |v103|
	v_mul_f32_e32 v114, 0x3fb8aa3b, v114
	v_exp_f32_e32 v114, v114
	s_nop 0
	v_add_f32_e32 v114, 1.0, v114
	v_rcp_f32_e32 v114, v114
	s_nop 0
	v_fma_f32 v114, v114, -2.0, 1.0
	v_add_f32_e64 v115, |v108|, |v108|
	v_mul_f32_e32 v115, 0x3fb8aa3b, v115
	v_exp_f32_e32 v115, v115
	s_nop 0
	v_add_f32_e32 v115, 1.0, v115
	v_rcp_f32_e32 v115, v115
	s_nop 0
	v_fma_f32 v115, v115, -2.0, 1.0
	v_add_f32_e64 v116, |v109|, |v109|
	v_mul_f32_e32 v116, 0x3fb8aa3b, v116
	v_exp_f32_e32 v116, v116
	s_nop 0
	v_add_f32_e32 v116, 1.0, v116
	v_rcp_f32_e32 v116, v116
	s_nop 0
	v_fma_f32 v116, v116, -2.0, 1.0
	v_add_f32_e64 v117, |v104|, |v104|
	v_mul_f32_e32 v117, 0x3fb8aa3b, v117
	v_exp_f32_e32 v117, v117
	s_nop 0
	v_add_f32_e32 v117, 1.0, v117
	v_rcp_f32_e32 v117, v117
	s_nop 0
	v_fma_f32 v117, v117, -2.0, 1.0
	v_add_f32_e64 v118, |v105|, |v105|
	v_mul_f32_e32 v118, 0x3fb8aa3b, v118
	v_exp_f32_e32 v118, v118
	s_nop 0
	v_add_f32_e32 v118, 1.0, v118
	v_rcp_f32_e32 v118, v118
	s_nop 0
	v_fma_f32 v118, v118, -2.0, 1.0
	v_bfi_b32 v106, s85, v110, v106
	v_bfi_b32 v107, s85, v111, v107
	v_bfi_b32 v102, s85, v113, v102
	v_bfi_b32 v103, s85, v114, v103
	v_bfi_b32 v108, s85, v115, v108
	v_bfi_b32 v109, s85, v116, v109
	v_bfi_b32 v104, s85, v117, v104
	v_bfi_b32 v105, s85, v118, v105

.LBB0_589:
	s_andn2_saveexec_b64 s[40:41], s[40:41]
	s_cbranch_execz .LBB0_623
	v_add_f32_e64 v106, |v102|, |v102|
	v_mul_f32_e32 v106, 0x3fb8aa3b, v106
	v_exp_f32_e32 v106, v106
	s_nop 0
	v_add_f32_e32 v106, 1.0, v106
	v_rcp_f32_e32 v106, v106
	s_nop 0
	v_fma_f32 v106, v106, -2.0, 1.0
	v_add_f32_e64 v107, |v103|, |v103|
	v_mul_f32_e32 v107, 0x3fb8aa3b, v107
	v_exp_f32_e32 v107, v107
	s_nop 0
	v_add_f32_e32 v107, 1.0, v107
	v_rcp_f32_e32 v107, v107
	s_nop 0
	v_fma_f32 v107, v107, -2.0, 1.0
	v_add_f32_e64 v109, |v98|, |v98|
	v_mul_f32_e32 v109, 0x3fb8aa3b, v109
	v_exp_f32_e32 v109, v109
	s_nop 0
	v_add_f32_e32 v109, 1.0, v109
	v_rcp_f32_e32 v109, v109
	s_nop 0
	v_fma_f32 v109, v109, -2.0, 1.0
	v_add_f32_e64 v110, |v99|, |v99|
	v_mul_f32_e32 v110, 0x3fb8aa3b, v110
	v_exp_f32_e32 v110, v110
	s_nop 0
	v_add_f32_e32 v110, 1.0, v110
	v_rcp_f32_e32 v110, v110
	s_nop 0
	v_fma_f32 v110, v110, -2.0, 1.0
	v_add_f32_e64 v111, |v104|, |v104|
	v_mul_f32_e32 v111, 0x3fb8aa3b, v111
	v_exp_f32_e32 v111, v111
	s_nop 0
	v_add_f32_e32 v111, 1.0, v111
	v_rcp_f32_e32 v111, v111
	s_nop 0
	v_fma_f32 v111, v111, -2.0, 1.0
	v_add_f32_e64 v112, |v105|, |v105|
	v_mul_f32_e32 v112, 0x3fb8aa3b, v112
	v_exp_f32_e32 v112, v112
	s_nop 0
	v_add_f32_e32 v112, 1.0, v112
	v_rcp_f32_e32 v112, v112
	s_nop 0
	v_fma_f32 v112, v112, -2.0, 1.0
	v_add_f32_e64 v113, |v100|, |v100|
	v_mul_f32_e32 v113, 0x3fb8aa3b, v113
	v_exp_f32_e32 v113, v113
	s_nop 0
	v_add_f32_e32 v113, 1.0, v113
	v_rcp_f32_e32 v113, v113
	s_nop 0
	v_fma_f32 v113, v113, -2.0, 1.0
	v_add_f32_e64 v114, |v101|, |v101|
	v_mul_f32_e32 v114, 0x3fb8aa3b, v114
	v_exp_f32_e32 v114, v114
	s_nop 0
	v_add_f32_e32 v114, 1.0, v114
	v_rcp_f32_e32 v114, v114
	s_nop 0
	v_fma_f32 v114, v114, -2.0, 1.0
	v_bfi_b32 v102, s85, v106, v102
	v_bfi_b32 v103, s85, v107, v103
	v_bfi_b32 v98, s85, v109, v98
	v_bfi_b32 v99, s85, v110, v99
	v_bfi_b32 v104, s85, v111, v104
	v_bfi_b32 v105, s85, v112, v105
	v_bfi_b32 v100, s85, v113, v100
	v_bfi_b32 v101, s85, v114, v101

.LBB0_640:
	s_andn2_saveexec_b64 s[18:19], s[18:19]
	s_cbranch_execz .LBB0_674
	v_add_f32_e64 v102, |v98|, |v98|
	v_mul_f32_e32 v102, 0x3fb8aa3b, v102
	v_exp_f32_e32 v102, v102
	s_nop 0
	v_add_f32_e32 v102, 1.0, v102
	v_rcp_f32_e32 v102, v102
	s_nop 0
	v_fma_f32 v102, v102, -2.0, 1.0
	v_add_f32_e64 v103, |v99|, |v99|
	v_mul_f32_e32 v103, 0x3fb8aa3b, v103
	v_exp_f32_e32 v103, v103
	s_nop 0
	v_add_f32_e32 v103, 1.0, v103
	v_rcp_f32_e32 v103, v103
	s_nop 0
	v_fma_f32 v103, v103, -2.0, 1.0
	v_add_f32_e64 v105, |v94|, |v94|
	v_mul_f32_e32 v105, 0x3fb8aa3b, v105
	v_exp_f32_e32 v105, v105
	s_nop 0
	v_add_f32_e32 v105, 1.0, v105
	v_rcp_f32_e32 v105, v105
	s_nop 0
	v_fma_f32 v105, v105, -2.0, 1.0
	v_add_f32_e64 v106, |v95|, |v95|
	v_mul_f32_e32 v106, 0x3fb8aa3b, v106
	v_exp_f32_e32 v106, v106
	s_nop 0
	v_add_f32_e32 v106, 1.0, v106
	v_rcp_f32_e32 v106, v106
	s_nop 0
	v_fma_f32 v106, v106, -2.0, 1.0
	v_add_f32_e64 v107, |v100|, |v100|
	v_mul_f32_e32 v107, 0x3fb8aa3b, v107
	v_exp_f32_e32 v107, v107
	s_nop 0
	v_add_f32_e32 v107, 1.0, v107
	v_rcp_f32_e32 v107, v107
	s_nop 0
	v_fma_f32 v107, v107, -2.0, 1.0
	v_add_f32_e64 v108, |v101|, |v101|
	v_mul_f32_e32 v108, 0x3fb8aa3b, v108
	v_exp_f32_e32 v108, v108
	s_nop 0
	v_add_f32_e32 v108, 1.0, v108
	v_rcp_f32_e32 v108, v108
	s_nop 0
	v_fma_f32 v108, v108, -2.0, 1.0
	v_add_f32_e64 v109, |v96|, |v96|
	v_mul_f32_e32 v109, 0x3fb8aa3b, v109
	v_exp_f32_e32 v109, v109
	s_nop 0
	v_add_f32_e32 v109, 1.0, v109
	v_rcp_f32_e32 v109, v109
	s_nop 0
	v_fma_f32 v109, v109, -2.0, 1.0
	v_add_f32_e64 v110, |v97|, |v97|
	v_mul_f32_e32 v110, 0x3fb8aa3b, v110
	v_exp_f32_e32 v110, v110
	s_nop 0
	v_add_f32_e32 v110, 1.0, v110
	v_rcp_f32_e32 v110, v110
	s_nop 0
	v_fma_f32 v110, v110, -2.0, 1.0
	v_bfi_b32 v98, s85, v102, v98
	v_bfi_b32 v99, s85, v103, v99
	v_bfi_b32 v94, s85, v105, v94
	v_bfi_b32 v95, s85, v106, v95
	v_bfi_b32 v100, s85, v107, v100
	v_bfi_b32 v101, s85, v108, v101
	v_bfi_b32 v96, s85, v109, v96
	v_bfi_b32 v97, s85, v110, v97

.LBB0_691:
	s_andn2_saveexec_b64 s[16:17], s[16:17]
	s_cbranch_execz .LBB0_725
	v_add_f32_e64 v98, |v94|, |v94|
	v_mul_f32_e32 v98, 0x3fb8aa3b, v98
	v_exp_f32_e32 v98, v98
	s_nop 0
	v_add_f32_e32 v98, 1.0, v98
	v_rcp_f32_e32 v98, v98
	s_nop 0
	v_fma_f32 v98, v98, -2.0, 1.0
	v_add_f32_e64 v99, |v95|, |v95|
	v_mul_f32_e32 v99, 0x3fb8aa3b, v99
	v_exp_f32_e32 v99, v99
	s_nop 0
	v_add_f32_e32 v99, 1.0, v99
	v_rcp_f32_e32 v99, v99
	s_nop 0
	v_fma_f32 v99, v99, -2.0, 1.0
	v_add_f32_e64 v101, |v90|, |v90|
	v_mul_f32_e32 v101, 0x3fb8aa3b, v101
	v_exp_f32_e32 v101, v101
	s_nop 0
	v_add_f32_e32 v101, 1.0, v101
	v_rcp_f32_e32 v101, v101
	s_nop 0
	v_fma_f32 v101, v101, -2.0, 1.0
	v_add_f32_e64 v102, |v91|, |v91|
	v_mul_f32_e32 v102, 0x3fb8aa3b, v102
	v_exp_f32_e32 v102, v102
	s_nop 0
	v_add_f32_e32 v102, 1.0, v102
	v_rcp_f32_e32 v102, v102
	s_nop 0
	v_fma_f32 v102, v102, -2.0, 1.0
	v_add_f32_e64 v103, |v96|, |v96|
	v_mul_f32_e32 v103, 0x3fb8aa3b, v103
	v_exp_f32_e32 v103, v103
	s_nop 0
	v_add_f32_e32 v103, 1.0, v103
	v_rcp_f32_e32 v103, v103
	s_nop 0
	v_fma_f32 v103, v103, -2.0, 1.0
	v_add_f32_e64 v104, |v97|, |v97|
	v_mul_f32_e32 v104, 0x3fb8aa3b, v104
	v_exp_f32_e32 v104, v104
	s_nop 0
	v_add_f32_e32 v104, 1.0, v104
	v_rcp_f32_e32 v104, v104
	s_nop 0
	v_fma_f32 v104, v104, -2.0, 1.0
	v_add_f32_e64 v105, |v92|, |v92|
	v_mul_f32_e32 v105, 0x3fb8aa3b, v105
	v_exp_f32_e32 v105, v105
	s_nop 0
	v_add_f32_e32 v105, 1.0, v105
	v_rcp_f32_e32 v105, v105
	s_nop 0
	v_fma_f32 v105, v105, -2.0, 1.0
	v_add_f32_e64 v106, |v93|, |v93|
	v_mul_f32_e32 v106, 0x3fb8aa3b, v106
	v_exp_f32_e32 v106, v106
	s_nop 0
	v_add_f32_e32 v106, 1.0, v106
	v_rcp_f32_e32 v106, v106
	s_nop 0
	v_fma_f32 v106, v106, -2.0, 1.0
	v_bfi_b32 v94, s85, v98, v94
	v_bfi_b32 v95, s85, v99, v95
	v_bfi_b32 v90, s85, v101, v90
	v_bfi_b32 v91, s85, v102, v91
	v_bfi_b32 v96, s85, v103, v96
	v_bfi_b32 v97, s85, v104, v97
	v_bfi_b32 v92, s85, v105, v92
	v_bfi_b32 v93, s85, v106, v93

.LBB0_742:
	s_andn2_saveexec_b64 s[14:15], s[14:15]
	s_cbranch_execz .LBB0_776
	v_add_f32_e64 v94, |v90|, |v90|
	v_mul_f32_e32 v94, 0x3fb8aa3b, v94
	v_exp_f32_e32 v94, v94
	s_nop 0
	v_add_f32_e32 v94, 1.0, v94
	v_rcp_f32_e32 v94, v94
	s_nop 0
	v_fma_f32 v94, v94, -2.0, 1.0
	v_add_f32_e64 v95, |v91|, |v91|
	v_mul_f32_e32 v95, 0x3fb8aa3b, v95
	v_exp_f32_e32 v95, v95
	s_nop 0
	v_add_f32_e32 v95, 1.0, v95
	v_rcp_f32_e32 v95, v95
	s_nop 0
	v_fma_f32 v95, v95, -2.0, 1.0
	v_add_f32_e64 v97, |v86|, |v86|
	v_mul_f32_e32 v97, 0x3fb8aa3b, v97
	v_exp_f32_e32 v97, v97
	s_nop 0
	v_add_f32_e32 v97, 1.0, v97
	v_rcp_f32_e32 v97, v97
	s_nop 0
	v_fma_f32 v97, v97, -2.0, 1.0
	v_add_f32_e64 v98, |v87|, |v87|
	v_mul_f32_e32 v98, 0x3fb8aa3b, v98
	v_exp_f32_e32 v98, v98
	s_nop 0
	v_add_f32_e32 v98, 1.0, v98
	v_rcp_f32_e32 v98, v98
	s_nop 0
	v_fma_f32 v98, v98, -2.0, 1.0
	v_add_f32_e64 v99, |v92|, |v92|
	v_mul_f32_e32 v99, 0x3fb8aa3b, v99
	v_exp_f32_e32 v99, v99
	s_nop 0
	v_add_f32_e32 v99, 1.0, v99
	v_rcp_f32_e32 v99, v99
	s_nop 0
	v_fma_f32 v99, v99, -2.0, 1.0
	v_add_f32_e64 v100, |v93|, |v93|
	v_mul_f32_e32 v100, 0x3fb8aa3b, v100
	v_exp_f32_e32 v100, v100
	s_nop 0
	v_add_f32_e32 v100, 1.0, v100
	v_rcp_f32_e32 v100, v100
	s_nop 0
	v_fma_f32 v100, v100, -2.0, 1.0
	v_add_f32_e64 v101, |v88|, |v88|
	v_mul_f32_e32 v101, 0x3fb8aa3b, v101
	v_exp_f32_e32 v101, v101
	s_nop 0
	v_add_f32_e32 v101, 1.0, v101
	v_rcp_f32_e32 v101, v101
	s_nop 0
	v_fma_f32 v101, v101, -2.0, 1.0
	v_add_f32_e64 v102, |v89|, |v89|
	v_mul_f32_e32 v102, 0x3fb8aa3b, v102
	v_exp_f32_e32 v102, v102
	s_nop 0
	v_add_f32_e32 v102, 1.0, v102
	v_rcp_f32_e32 v102, v102
	s_nop 0
	v_fma_f32 v102, v102, -2.0, 1.0
	v_bfi_b32 v90, s85, v94, v90
	v_bfi_b32 v91, s85, v95, v91
	v_bfi_b32 v86, s85, v97, v86
	v_bfi_b32 v87, s85, v98, v87
	v_bfi_b32 v92, s85, v99, v92
	v_bfi_b32 v93, s85, v100, v93
	v_bfi_b32 v88, s85, v101, v88
	v_bfi_b32 v89, s85, v102, v89

.LBB0_794:
	s_waitcnt vmcnt(0)
	v_lshlrev_b32_e32 v26, 16, v14
	v_mul_f32_e32 v27, 0x3d372713, v26
	v_mul_f32_e32 v27, v27, v26
	v_fma_f32 v27, v27, v26, v26
	v_mul_f32_e32 v27, 0x3f4c422a, v27
	v_add_f32_e64 v28, |v27|, |v27|
	v_mul_f32_e32 v28, 0x3fb8aa3b, v28
	v_exp_f32_e32 v28, v28
	s_nop 0
	v_add_f32_e32 v28, 1.0, v28
	v_rcp_f32_e32 v28, v28
	s_nop 0
	v_fma_f32 v28, v28, -2.0, 1.0
	v_and_b32_e32 v14, 0xffff0000, v14
	v_mul_f32_e32 v29, 0x3d372713, v14
	v_mul_f32_e32 v29, v29, v14
	v_fma_f32 v29, v29, v14, v14
	v_mul_f32_e32 v29, 0x3f4c422a, v29
	v_add_f32_e64 v30, |v29|, |v29|
	v_mul_f32_e32 v30, 0x3fb8aa3b, v30
	v_exp_f32_e32 v30, v30
	s_nop 0
	v_add_f32_e32 v30, 1.0, v30
	v_rcp_f32_e32 v30, v30
	s_nop 0
	v_fma_f32 v30, v30, -2.0, 1.0
	v_lshlrev_b32_e32 v31, 16, v15
	v_mul_f32_e32 v32, 0x3d372713, v31
	v_mul_f32_e32 v32, v32, v31
	v_fma_f32 v32, v32, v31, v31
	v_mul_f32_e32 v32, 0x3f4c422a, v32
	v_add_f32_e64 v33, |v32|, |v32|
	v_mul_f32_e32 v33, 0x3fb8aa3b, v33
	v_exp_f32_e32 v33, v33
	s_nop 0
	v_add_f32_e32 v33, 1.0, v33
	v_rcp_f32_e32 v33, v33
	s_nop 0
	v_fma_f32 v33, v33, -2.0, 1.0
	v_and_b32_e32 v15, 0xffff0000, v15
	v_mul_f32_e32 v34, 0x3d372713, v15
	v_mul_f32_e32 v34, v34, v15
	v_fma_f32 v34, v34, v15, v15
	v_mul_f32_e32 v34, 0x3f4c422a, v34
	v_add_f32_e64 v35, |v34|, |v34|
	v_mul_f32_e32 v35, 0x3fb8aa3b, v35
	v_exp_f32_e32 v35, v35
	s_nop 0
	v_add_f32_e32 v35, 1.0, v35
	v_rcp_f32_e32 v35, v35
	s_nop 0
	v_fma_f32 v35, v35, -2.0, 1.0
	v_lshlrev_b32_e32 v36, 16, v16
	v_mul_f32_e32 v37, 0x3d372713, v36
	v_mul_f32_e32 v37, v37, v36
	v_fma_f32 v37, v37, v36, v36
	v_mul_f32_e32 v37, 0x3f4c422a, v37
	v_add_f32_e64 v38, |v37|, |v37|
	v_mul_f32_e32 v38, 0x3fb8aa3b, v38
	v_exp_f32_e32 v38, v38
	s_nop 0
	v_add_f32_e32 v38, 1.0, v38
	v_rcp_f32_e32 v38, v38
	s_nop 0
	v_fma_f32 v38, v38, -2.0, 1.0
	v_and_b32_e32 v16, 0xffff0000, v16
	v_mul_f32_e32 v39, 0x3d372713, v16
	v_mul_f32_e32 v39, v39, v16
	v_fma_f32 v39, v39, v16, v16
	v_mul_f32_e32 v39, 0x3f4c422a, v39
	v_add_f32_e64 v40, |v39|, |v39|
	v_mul_f32_e32 v40, 0x3fb8aa3b, v40
	v_exp_f32_e32 v40, v40
	s_nop 0
	v_add_f32_e32 v40, 1.0, v40
	v_rcp_f32_e32 v40, v40
	s_nop 0
	v_fma_f32 v40, v40, -2.0, 1.0
	v_lshlrev_b32_e32 v41, 16, v17
	v_mul_f32_e32 v42, 0x3d372713, v41
	v_mul_f32_e32 v42, v42, v41
	v_fma_f32 v42, v42, v41, v41
	v_mul_f32_e32 v42, 0x3f4c422a, v42
	v_add_f32_e64 v43, |v42|, |v42|
	v_mul_f32_e32 v43, 0x3fb8aa3b, v43
	v_exp_f32_e32 v43, v43
	s_nop 0
	v_add_f32_e32 v43, 1.0, v43
	v_rcp_f32_e32 v43, v43
	s_nop 0
	v_fma_f32 v43, v43, -2.0, 1.0
	v_and_b32_e32 v17, 0xffff0000, v17
	v_mul_f32_e32 v44, 0x3d372713, v17
	v_mul_f32_e32 v44, v44, v17
	v_fma_f32 v44, v44, v17, v17
	v_mul_f32_e32 v44, 0x3f4c422a, v44
	v_add_f32_e64 v45, |v44|, |v44|
	v_mul_f32_e32 v45, 0x3fb8aa3b, v45
	v_exp_f32_e32 v45, v45
	s_nop 0
	v_add_f32_e32 v45, 1.0, v45
	v_rcp_f32_e32 v45, v45
	s_nop 0
	v_fma_f32 v45, v45, -2.0, 1.0
	v_lshlrev_b32_e32 v46, 16, v10
	v_mul_f32_e32 v47, 0x3d372713, v46
	v_mul_f32_e32 v47, v47, v46
	v_fma_f32 v47, v47, v46, v46
	v_mul_f32_e32 v47, 0x3f4c422a, v47
	v_add_f32_e64 v48, |v47|, |v47|
	v_mul_f32_e32 v48, 0x3fb8aa3b, v48
	v_exp_f32_e32 v48, v48
	s_nop 0
	v_add_f32_e32 v48, 1.0, v48
	v_rcp_f32_e32 v48, v48
	s_nop 0
	v_fma_f32 v48, v48, -2.0, 1.0
	v_and_b32_e32 v10, 0xffff0000, v10
	v_mul_f32_e32 v49, 0x3d372713, v10
	v_mul_f32_e32 v49, v49, v10
	v_fma_f32 v49, v49, v10, v10
	v_mul_f32_e32 v49, 0x3f4c422a, v49
	v_cmp_nlt_f32_e64 s[0:1], |v49|, s13
	s_and_saveexec_b64 s[26:27], s[0:1]
	s_xor_b64 s[0:1], exec, s[26:27]
	s_cbranch_execz .LBB0_832
	v_add_f32_e64 v55, |v49|, |v49|
	s_waitcnt lgkmcnt(0)
	v_mul_f32_e32 v56, 0x3fb8aa3b, v55
	v_rndne_f32_e32 v57, v56
	v_sub_f32_e32 v58, v56, v57
	v_fma_f32 v56, v55, s14, -v56
	v_fmac_f32_e32 v56, 0x32a5705f, v55
	v_add_f32_e32 v56, v58, v56
	v_cvt_i32_f32_e32 v57, v57
	v_exp_f32_e32 v56, v56
	v_cmp_ngt_f32_e32 vcc, s15, v55
	v_ldexp_f32 v56, v56, v57
	s_nop 0
	v_cndmask_b32_e32 v56, 0, v56, vcc
	v_cmp_nlt_f32_e32 vcc, s16, v55
	s_nop 1
	v_cndmask_b32_e32 v55, v54, v56, vcc
	v_add_f32_e32 v55, 1.0, v55
	v_rcp_f32_e32 v55, v55
	s_nop 0
	v_fma_f32 v55, v55, -2.0, 1.0

.LBB0_834:
	s_or_b64 exec, exec, s[0:1]
	s_waitcnt lgkmcnt(0)
	v_lshlrev_b32_e32 v56, 16, v11
	v_mul_f32_e32 v57, 0x3d372713, v56
	v_mul_f32_e32 v57, v57, v56
	v_fma_f32 v57, v57, v56, v56
	v_mul_f32_e32 v57, 0x3f4c422a, v57
	v_add_f32_e64 v58, |v57|, |v57|
	v_mul_f32_e32 v58, 0x3fb8aa3b, v58
	v_exp_f32_e32 v58, v58
	s_nop 0
	v_add_f32_e32 v58, 1.0, v58
	v_rcp_f32_e32 v58, v58
	s_nop 0
	v_fma_f32 v58, v58, -2.0, 1.0
	v_and_b32_e32 v11, 0xffff0000, v11
	v_mul_f32_e32 v59, 0x3d372713, v11
	v_mul_f32_e32 v59, v59, v11
	v_fma_f32 v59, v59, v11, v11
	v_mul_f32_e32 v59, 0x3f4c422a, v59
	v_add_f32_e64 v60, |v59|, |v59|
	v_mul_f32_e32 v60, 0x3fb8aa3b, v60
	v_exp_f32_e32 v60, v60
	s_nop 0
	v_add_f32_e32 v60, 1.0, v60
	v_rcp_f32_e32 v60, v60
	s_nop 0
	v_fma_f32 v60, v60, -2.0, 1.0
	v_lshlrev_b32_e32 v61, 16, v12
	v_mul_f32_e32 v62, 0x3d372713, v61
	v_mul_f32_e32 v62, v62, v61
	v_fma_f32 v62, v62, v61, v61
	v_mul_f32_e32 v62, 0x3f4c422a, v62
	v_add_f32_e64 v63, |v62|, |v62|
	v_mul_f32_e32 v63, 0x3fb8aa3b, v63
	v_exp_f32_e32 v63, v63
	s_nop 0
	v_add_f32_e32 v63, 1.0, v63
	v_rcp_f32_e32 v63, v63
	s_nop 0
	v_fma_f32 v63, v63, -2.0, 1.0
	v_and_b32_e32 v12, 0xffff0000, v12
	v_mul_f32_e32 v64, 0x3d372713, v12
	v_mul_f32_e32 v64, v64, v12
	v_fma_f32 v64, v64, v12, v12
	v_mul_f32_e32 v64, 0x3f4c422a, v64
	v_add_f32_e64 v65, |v64|, |v64|
	v_mul_f32_e32 v65, 0x3fb8aa3b, v65
	v_exp_f32_e32 v65, v65
	s_nop 0
	v_add_f32_e32 v65, 1.0, v65
	v_rcp_f32_e32 v65, v65
	s_nop 0
	v_fma_f32 v65, v65, -2.0, 1.0
	v_lshlrev_b32_e32 v66, 16, v13
	v_mul_f32_e32 v67, 0x3d372713, v66
	v_mul_f32_e32 v67, v67, v66
	v_fma_f32 v67, v67, v66, v66
	v_mul_f32_e32 v67, 0x3f4c422a, v67
	v_add_f32_e64 v68, |v67|, |v67|
	v_mul_f32_e32 v68, 0x3fb8aa3b, v68
	v_exp_f32_e32 v68, v68
	s_nop 0
	v_add_f32_e32 v68, 1.0, v68
	v_rcp_f32_e32 v68, v68
	s_nop 0
	v_fma_f32 v68, v68, -2.0, 1.0
	v_and_b32_e32 v13, 0xffff0000, v13
	v_mul_f32_e32 v69, 0x3d372713, v13
	v_mul_f32_e32 v69, v69, v13
	v_fma_f32 v69, v69, v13, v13
	v_mul_f32_e32 v69, 0x3f4c422a, v69
	v_add_f32_e64 v70, |v69|, |v69|
	v_mul_f32_e32 v70, 0x3fb8aa3b, v70
	v_exp_f32_e32 v70, v70
	s_nop 0
	v_add_f32_e32 v70, 1.0, v70
	v_rcp_f32_e32 v70, v70
	s_nop 0
	v_fma_f32 v70, v70, -2.0, 1.0
	v_lshlrev_b32_e32 v71, 16, v6
	v_mul_f32_e32 v72, 0x3d372713, v71
	v_mul_f32_e32 v72, v72, v71
	v_fma_f32 v72, v72, v71, v71
	v_mul_f32_e32 v72, 0x3f4c422a, v72
	v_add_f32_e64 v73, |v72|, |v72|
	v_mul_f32_e32 v73, 0x3fb8aa3b, v73
	v_exp_f32_e32 v73, v73
	s_nop 0
	v_add_f32_e32 v73, 1.0, v73
	v_rcp_f32_e32 v73, v73
	s_nop 0
	v_fma_f32 v73, v73, -2.0, 1.0
	v_and_b32_e32 v74, 0xffff0000, v6
	v_mul_f32_e32 v6, 0x3d372713, v74
	v_mul_f32_e32 v6, v6, v74
	v_fma_f32 v6, v6, v74, v74
	v_mul_f32_e32 v75, 0x3f4c422a, v6
	v_cmp_nlt_f32_e64 s[0:1], |v75|, s13
	s_and_saveexec_b64 s[26:27], s[0:1]
	s_xor_b64 s[0:1], exec, s[26:27]
	s_cbranch_execz .LBB0_864
	v_add_f32_e64 v6, |v75|, |v75|
	v_mul_f32_e32 v76, 0x3fb8aa3b, v6
	v_rndne_f32_e32 v77, v76
	v_sub_f32_e32 v78, v76, v77
	v_fma_f32 v76, v6, s14, -v76
	v_fmac_f32_e32 v76, 0x32a5705f, v6
	v_add_f32_e32 v76, v78, v76
	v_cvt_i32_f32_e32 v77, v77
	v_exp_f32_e32 v76, v76
	v_cmp_ngt_f32_e32 vcc, s15, v6
	v_ldexp_f32 v76, v76, v77
	s_nop 0
	v_cndmask_b32_e32 v76, 0, v76, vcc
	v_cmp_nlt_f32_e32 vcc, s16, v6
	s_nop 1
	v_cndmask_b32_e32 v6, v54, v76, vcc
	v_add_f32_e32 v6, 1.0, v6
	v_rcp_f32_e32 v6, v6
	s_nop 0
	v_fma_f32 v76, v6, -2.0, 1.0

.LBB0_888:
	s_andn2_saveexec_b64 s[0:1], s[0:1]
	v_mul_f32_e32 v6, v91, v91
	v_fmamk_f32 v7, v6, 0xbbbac73d, v51
	v_fmaak_f32 v7, v6, v7, 0xbd5c1c4e
	v_fmaak_f32 v7, v6, v7, 0x3e088382
	v_fmaak_f32 v7, v6, v7, 0xbeaaaa99
	v_mul_f32_e64 v7, |v91|, v7
	v_fma_f32 v92, v6, v7, |v91|
	s_or_b64 exec, exec, s[0:1]
	v_lshlrev_b32_e32 v6, 16, v2
	v_mul_f32_e32 v7, 0x3d372713, v6
	v_mul_f32_e32 v7, v7, v6
	v_fma_f32 v7, v7, v6, v6
	v_mul_f32_e32 v7, 0x3f4c422a, v7
	v_add_f32_e64 v93, |v7|, |v7|
	v_mul_f32_e32 v93, 0x3fb8aa3b, v93
	v_exp_f32_e32 v93, v93
	s_nop 0
	v_add_f32_e32 v93, 1.0, v93
	v_rcp_f32_e32 v93, v93
	s_nop 0
	v_fma_f32 v93, v93, -2.0, 1.0
	v_and_b32_e32 v94, 0xffff0000, v2
	v_mul_f32_e32 v2, 0x3d372713, v94
	v_mul_f32_e32 v2, v2, v94
	v_fma_f32 v2, v2, v94, v94
	v_mul_f32_e32 v95, 0x3f4c422a, v2
	v_cmp_nlt_f32_e64 s[0:1], |v95|, s13
	s_and_saveexec_b64 s[26:27], s[0:1]
	s_xor_b64 s[0:1], exec, s[26:27]
	s_cbranch_execz .LBB0_896
	v_add_f32_e64 v2, |v95|, |v95|
	v_mul_f32_e32 v96, 0x3fb8aa3b, v2
	v_rndne_f32_e32 v97, v96
	v_sub_f32_e32 v98, v96, v97
	v_fma_f32 v96, v2, s14, -v96
	v_fmac_f32_e32 v96, 0x32a5705f, v2
	v_add_f32_e32 v96, v98, v96
	v_cvt_i32_f32_e32 v97, v97
	v_exp_f32_e32 v96, v96
	v_cmp_ngt_f32_e32 vcc, s15, v2
	v_ldexp_f32 v96, v96, v97
	s_nop 0
	v_cndmask_b32_e32 v96, 0, v96, vcc
	v_cmp_nlt_f32_e32 vcc, s16, v2
	s_nop 1
	v_cndmask_b32_e32 v2, v54, v96, vcc
	v_add_f32_e32 v2, 1.0, v2
	v_rcp_f32_e32 v2, v2
	s_nop 0
	v_fma_f32 v96, v2, -2.0, 1.0

.LBB0_1006:
	ds_read_b64_tr_b16 v[82:83], v154
	ds_read_b64_tr_b16 v[86:87], v154 offset:32
	ds_read_b64_tr_b16 v[84:85], v145 offset:576
	ds_read_b64_tr_b16 v[88:89], v145 offset:608
	ds_read_b64_tr_b16 v[90:91], v154 offset:64
	ds_read_b64_tr_b16 v[92:93], v145 offset:640
	ds_read_b64_tr_b16 v[94:95], v154 offset:96
	ds_read_b64_tr_b16 v[96:97], v145 offset:672
	ds_read_b128 v[98:101], v155 offset:18432
	ds_read_b128 v[134:137], v155 offset:22784
	s_add_i32 s2, s22, s14
	s_ashr_i32 s3, s2, 31
	s_lshr_b32 s3, s3, 25
	s_waitcnt lgkmcnt(1)
	v_mfma_f32_16x16x32_bf16 v[102:105], v[82:85], v[98:101], 0
	s_add_i32 s3, s2, s3
	s_and_b32 s16, s3, 0xffffff80
	s_sub_i32 s14, s2, s16
	v_mfma_f32_16x16x32_bf16 v[106:109], v[86:89], v[98:101], 0
	s_ashr_i32 s15, s14, 31
	s_lshl_b64 s[14:15], s[14:15], 7
	s_ashr_i32 s17, s3, 7
	v_mfma_f32_16x16x32_bf16 v[110:113], v[90:93], v[98:101], 0
	s_lshl_b32 s18, s17, 6
	s_ashr_i32 s19, s18, 31
	v_mfma_f32_16x16x32_bf16 v[98:101], v[94:97], v[98:101], 0
	s_waitcnt lgkmcnt(0)
	v_mfma_f32_16x16x32_bf16 v[82:85], v[82:85], v[134:137], 0
	v_mfma_f32_16x16x32_bf16 v[86:89], v[86:89], v[134:137], 0
	v_mfma_f32_16x16x32_bf16 v[90:93], v[90:93], v[134:137], 0
	v_mfma_f32_16x16x32_bf16 v[94:97], v[94:97], v[134:137], 0
	ds_read_b64_tr_b16 v[134:135], v154 offset:4608
	ds_read_b64_tr_b16 v[136:137], v145 offset:5184
	ds_read_b64_tr_b16 v[138:139], v154 offset:4640
	ds_read_b64_tr_b16 v[140:141], v145 offset:5216
	ds_read_b64_tr_b16 v[160:161], v154 offset:4672
	ds_read_b64_tr_b16 v[162:163], v145 offset:5248
	ds_read_b64_tr_b16 v[164:165], v154 offset:4704
	ds_read_b64_tr_b16 v[166:167], v145 offset:5280
	ds_read_b128 v[168:171], v155 offset:18496
	s_waitcnt lgkmcnt(0)
	v_mfma_f32_16x16x32_bf16 v[102:105], v[134:137], v[168:171], v[102:105]
	v_mfma_f32_16x16x32_bf16 v[106:109], v[138:141], v[168:171], v[106:109]
	v_mfma_f32_16x16x32_bf16 v[110:113], v[160:163], v[168:171], v[110:113]
	v_mfma_f32_16x16x32_bf16 v[98:101], v[164:167], v[168:171], v[98:101]
	ds_read_b128 v[168:171], v155 offset:22848
	s_waitcnt lgkmcnt(0)
	v_mfma_f32_16x16x32_bf16 v[82:85], v[134:137], v[168:171], v[82:85]
	v_mfma_f32_16x16x32_bf16 v[86:89], v[138:141], v[168:171], v[86:89]
	v_mfma_f32_16x16x32_bf16 v[90:93], v[160:163], v[168:171], v[90:93]
	v_mfma_f32_16x16x32_bf16 v[94:97], v[164:167], v[168:171], v[94:97]
	ds_read_b64_tr_b16 v[134:135], v154 offset:9216
	ds_read_b64_tr_b16 v[136:137], v145 offset:9792
	ds_read_b64_tr_b16 v[138:139], v154 offset:9248
	ds_read_b64_tr_b16 v[140:141], v145 offset:9824
	ds_read_b64_tr_b16 v[160:161], v154 offset:9280
	ds_read_b64_tr_b16 v[162:163], v145 offset:9856
	ds_read_b64_tr_b16 v[164:165], v154 offset:9312
	ds_read_b64_tr_b16 v[166:167], v145 offset:9888
	ds_read_b128 v[168:171], v155 offset:18560
	s_waitcnt lgkmcnt(0)
	v_mfma_f32_16x16x32_bf16 v[172:175], v[160:163], v[168:171], v[110:113]
	s_nop 2
	ds_read_b128 v[110:113], v155 offset:22912
	v_mfma_f32_16x16x32_bf16 v[102:105], v[134:137], v[168:171], v[102:105]
	v_mfma_f32_16x16x32_bf16 v[106:109], v[138:141], v[168:171], v[106:109]
	v_mfma_f32_16x16x32_bf16 v[98:101], v[164:167], v[168:171], v[98:101]
	s_waitcnt lgkmcnt(0)
	v_mfma_f32_16x16x32_bf16 v[82:85], v[134:137], v[110:113], v[82:85]
	v_mfma_f32_16x16x32_bf16 v[86:89], v[138:141], v[110:113], v[86:89]
	v_mfma_f32_16x16x32_bf16 v[134:137], v[160:163], v[110:113], v[90:93]
	v_mfma_f32_16x16x32_bf16 v[138:141], v[164:167], v[110:113], v[94:97]
	s_nop 1
	ds_read_b64_tr_b16 v[90:91], v154 offset:13824
	ds_read_b64_tr_b16 v[92:93], v145 offset:14400
	ds_read_b64_tr_b16 v[160:161], v154 offset:13856
	ds_read_b64_tr_b16 v[162:163], v145 offset:14432
	ds_read_b64_tr_b16 v[164:165], v154 offset:13888
	ds_read_b64_tr_b16 v[166:167], v145 offset:14464
	ds_read_b64_tr_b16 v[168:169], v154 offset:13920
	ds_read_b64_tr_b16 v[170:171], v145 offset:14496
	ds_read_b128 v[94:97], v155 offset:18624
	s_waitcnt lgkmcnt(0)
	v_mfma_f32_16x16x32_bf16 v[110:113], v[90:93], v[94:97], v[102:105]
	v_mfma_f32_16x16x32_bf16 v[102:105], v[164:167], v[94:97], v[172:175]
	s_nop 2
	ds_read_b128 v[172:175], v155 offset:22976
	v_mfma_f32_16x16x32_bf16 v[106:109], v[160:163], v[94:97], v[106:109]
	v_mfma_f32_16x16x32_bf16 v[98:101], v[168:171], v[94:97], v[98:101]
	s_waitcnt lgkmcnt(0)
	v_mfma_f32_16x16x32_bf16 v[94:97], v[90:93], v[172:175], v[82:85]
	v_mfma_f32_16x16x32_bf16 v[90:93], v[160:163], v[172:175], v[86:89]
	v_mfma_f32_16x16x32_bf16 v[86:89], v[164:167], v[172:175], v[134:137]
	v_mfma_f32_16x16x32_bf16 v[82:85], v[168:171], v[172:175], v[138:141]
	s_nop 1
	v_mov_b64_e32 v[136:137], s[0:1]
	v_or_b32_e32 v134, s16, v116
	v_ashrrev_i32_e32 v135, 31, v134
	v_or_b32_e32 v138, s14, v116
	v_mad_u64_u32 v[136:137], s[20:21], v138, s25, v[136:137]
	v_mad_i32_i24 v137, s15, v157, v137
	v_lshl_add_u64 v[136:137], s[18:19], 1, v[136:137]
	v_lshl_add_u64 v[136:137], v[136:137], 0, v[114:115]
	v_add_co_u32_e32 v140, vcc, 0x1000, v136
	v_lshl_add_u64 v[134:135], v[134:135], 2, s[4:5]
	s_nop 0
	v_addc_co_u32_e32 v141, vcc, 0, v137, vcc
	global_load_dwordx2 v[140:141], v[140:141], off offset:3968
	v_mov_b32_e32 v139, s15
	global_load_dword v134, v[134:135], off
	s_waitcnt vmcnt(1)
	v_lshlrev_b32_e32 v123, 16, v140
	v_mul_f32_e32 v125, 0x3d372713, v123
	v_mul_f32_e32 v125, v125, v123
	v_fma_f32 v125, v125, v123, v123
	v_mul_f32_e32 v125, 0x3f4c422a, v125
	v_add_f32_e64 v127, |v125|, |v125|
	v_mul_f32_e32 v127, 0x3fb8aa3b, v127
	v_exp_f32_e32 v127, v127
	s_nop 0
	v_add_f32_e32 v127, 1.0, v127
	v_rcp_f32_e32 v127, v127
	s_nop 0
	v_fma_f32 v127, v127, -2.0, 1.0
	v_and_b32_e32 v129, 0xffff0000, v140
	v_mul_f32_e32 v131, 0x3d372713, v129
	v_mul_f32_e32 v131, v131, v129
	v_fma_f32 v131, v131, v129, v129
	v_mul_f32_e32 v131, 0x3f4c422a, v131
	v_add_f32_e64 v132, |v131|, |v131|
	v_mul_f32_e32 v132, 0x3fb8aa3b, v132
	v_exp_f32_e32 v132, v132
	s_nop 0
	v_add_f32_e32 v132, 1.0, v132
	v_rcp_f32_e32 v132, v132
	s_nop 0
	v_fma_f32 v132, v132, -2.0, 1.0
	v_lshlrev_b32_e32 v135, 16, v141
	v_mul_f32_e32 v140, 0x3d372713, v135
	v_mul_f32_e32 v140, v140, v135
	v_fma_f32 v140, v140, v135, v135
	v_mul_f32_e32 v140, 0x3f4c422a, v140
	v_add_f32_e64 v159, |v140|, |v140|
	v_mul_f32_e32 v159, 0x3fb8aa3b, v159
	v_exp_f32_e32 v159, v159
	s_nop 0
	v_add_f32_e32 v159, 1.0, v159
	v_rcp_f32_e32 v159, v159
	s_nop 0
	v_fma_f32 v159, v159, -2.0, 1.0
	v_and_b32_e32 v141, 0xffff0000, v141
	v_mul_f32_e32 v160, 0x3d372713, v141
	v_mul_f32_e32 v160, v160, v141
	v_fma_f32 v160, v160, v141, v141
	v_mul_f32_e32 v160, 0x3f4c422a, v160
	v_add_f32_e64 v161, |v160|, |v160|
	v_mul_f32_e32 v161, 0x3fb8aa3b, v161
	v_exp_f32_e32 v161, v161
	s_nop 0
	v_add_f32_e32 v161, 1.0, v161
	v_rcp_f32_e32 v161, v161
	s_nop 0
	v_fma_f32 v161, v161, -2.0, 1.0
	v_bfi_b32 v140, s30, v159, v140
	v_mul_f32_e32 v135, 0.5, v135
	v_add_f32_e32 v140, 1.0, v140
	v_mul_f32_e32 v135, v135, v140
	s_waitcnt vmcnt(0)
	v_add_f32_e32 v112, v112, v134
	v_mul_f32_e32 v140, v112, v135
	v_mul_f32_e32 v112, 0.5, v123
	v_bfi_b32 v123, s30, v127, v125
	v_add_f32_e32 v123, 1.0, v123
	v_mul_f32_e32 v112, v112, v123
	v_add_f32_e32 v110, v110, v134
	v_bfi_b32 v135, s30, v132, v131
	v_mov_b32_e32 v132, v111
	v_mul_f32_e32 v112, v110, v112
	v_mul_f32_e32 v123, 0.5, v129
	v_pk_add_f32 v[110:111], v[132:133], v[134:135]
	v_bfi_b32 v135, s30, v161, v160
	v_mul_f32_e32 v111, v123, v111
	v_mul_f32_e32 v110, v110, v111
	v_mov_b32_e32 v132, v113
	v_cvt_pk_bf16_f32 v112, v112, v110
	v_lshlrev_b64 v[110:111], 12, v[138:139]
	v_mul_f32_e32 v123, 0.5, v141
	v_pk_add_f32 v[138:139], v[132:133], v[134:135]
	v_lshl_add_u64 v[110:111], s[8:9], 0, v[110:111]
	v_mul_f32_e32 v113, v123, v139
	v_lshl_add_u64 v[110:111], s[18:19], 1, v[110:111]
	v_mul_f32_e32 v113, v138, v113
	v_lshl_add_u64 v[136:137], v[136:137], 0, s[10:11]
	v_lshl_add_u64 v[110:111], v[110:111], 0, v[114:115]
	v_cvt_pk_bf16_f32 v113, v140, v113
	global_store_dwordx2 v[110:111], v[112:113], off offset:2048
	global_load_dwordx2 v[112:113], v[136:137], off offset:32
	s_waitcnt vmcnt(0)
	v_lshlrev_b32_e32 v123, 16, v112
	v_mul_f32_e32 v125, 0x3d372713, v123
	v_mul_f32_e32 v125, v125, v123
	v_fma_f32 v125, v125, v123, v123
	v_mul_f32_e32 v125, 0x3f4c422a, v125
	v_add_f32_e64 v127, |v125|, |v125|
	v_mul_f32_e32 v127, 0x3fb8aa3b, v127
	v_exp_f32_e32 v127, v127
	s_nop 0
	v_add_f32_e32 v127, 1.0, v127
	v_rcp_f32_e32 v127, v127
	s_nop 0
	v_fma_f32 v127, v127, -2.0, 1.0
	v_and_b32_e32 v112, 0xffff0000, v112
	v_mul_f32_e32 v129, 0x3d372713, v112
	v_mul_f32_e32 v129, v129, v112
	v_fma_f32 v129, v129, v112, v112
	v_mul_f32_e32 v129, 0x3f4c422a, v129
	v_add_f32_e64 v131, |v129|, |v129|
	v_mul_f32_e32 v131, 0x3fb8aa3b, v131
	v_exp_f32_e32 v131, v131
	s_nop 0
	v_add_f32_e32 v131, 1.0, v131
	v_rcp_f32_e32 v131, v131
	s_nop 0
	v_fma_f32 v131, v131, -2.0, 1.0
	v_lshlrev_b32_e32 v132, 16, v113
	v_mul_f32_e32 v135, 0x3d372713, v132
	v_mul_f32_e32 v135, v135, v132
	v_fma_f32 v135, v135, v132, v132
	v_mul_f32_e32 v135, 0x3f4c422a, v135
	v_add_f32_e64 v138, |v135|, |v135|
	v_mul_f32_e32 v138, 0x3fb8aa3b, v138
	v_exp_f32_e32 v138, v138
	s_nop 0
	v_add_f32_e32 v138, 1.0, v138
	v_rcp_f32_e32 v138, v138
	s_nop 0
	v_fma_f32 v138, v138, -2.0, 1.0
	v_and_b32_e32 v113, 0xffff0000, v113
	v_mul_f32_e32 v139, 0x3d372713, v113
	v_mul_f32_e32 v139, v139, v113
	v_fma_f32 v139, v139, v113, v113
	v_mul_f32_e32 v139, 0x3f4c422a, v139
	v_add_f32_e64 v140, |v139|, |v139|
	v_mul_f32_e32 v140, 0x3fb8aa3b, v140
	v_exp_f32_e32 v140, v140
	s_nop 0
	v_add_f32_e32 v140, 1.0, v140
	v_rcp_f32_e32 v140, v140
	s_nop 0
	v_fma_f32 v140, v140, -2.0, 1.0
	v_bfi_b32 v135, s30, v138, v135
	v_mul_f32_e32 v132, 0.5, v132
	v_add_f32_e32 v135, 1.0, v135
	v_mul_f32_e32 v132, v132, v135
	v_add_f32_e32 v108, v108, v134
	v_mul_f32_e32 v138, v108, v132
	v_mul_f32_e32 v108, 0.5, v123
	v_bfi_b32 v123, s30, v127, v125
	v_add_f32_e32 v123, 1.0, v123
	v_mul_f32_e32 v108, v108, v123
	v_add_f32_e32 v106, v106, v134
	v_bfi_b32 v135, s30, v131, v129
	v_mov_b32_e32 v132, v107
	v_mul_f32_e32 v108, v106, v108
	v_mul_f32_e32 v112, 0.5, v112
	v_pk_add_f32 v[106:107], v[132:133], v[134:135]
	v_bfi_b32 v135, s30, v140, v139
	v_mul_f32_e32 v107, v112, v107
	v_mul_f32_e32 v106, v106, v107
	v_mov_b32_e32 v132, v109
	v_cvt_pk_bf16_f32 v106, v108, v106
	v_mul_f32_e32 v107, 0.5, v113
	v_pk_add_f32 v[108:109], v[132:133], v[134:135]
	s_nop 0
	v_mul_f32_e32 v107, v107, v109
	v_mul_f32_e32 v107, v108, v107
	v_cvt_pk_bf16_f32 v107, v138, v107
	global_store_dwordx2 v[110:111], v[106:107], off offset:2080
	global_load_dwordx2 v[106:107], v[136:137], off offset:64
	s_waitcnt vmcnt(0)
	v_lshlrev_b32_e32 v108, 16, v106
	v_mul_f32_e32 v109, 0x3d372713, v108
	v_mul_f32_e32 v109, v109, v108
	v_fma_f32 v109, v109, v108, v108
	v_mul_f32_e32 v109, 0x3f4c422a, v109
	v_add_f32_e64 v112, |v109|, |v109|
	v_mul_f32_e32 v112, 0x3fb8aa3b, v112
	v_exp_f32_e32 v112, v112
	s_nop 0
	v_add_f32_e32 v112, 1.0, v112
	v_rcp_f32_e32 v112, v112
	s_nop 0
	v_fma_f32 v112, v112, -2.0, 1.0
	v_and_b32_e32 v106, 0xffff0000, v106
	v_mul_f32_e32 v113, 0x3d372713, v106
	v_mul_f32_e32 v113, v113, v106
	v_fma_f32 v113, v113, v106, v106
	v_mul_f32_e32 v113, 0x3f4c422a, v113
	v_add_f32_e64 v123, |v113|, |v113|
	v_mul_f32_e32 v123, 0x3fb8aa3b, v123
	v_exp_f32_e32 v123, v123
	s_nop 0
	v_add_f32_e32 v123, 1.0, v123
	v_rcp_f32_e32 v123, v123
	s_nop 0
	v_fma_f32 v123, v123, -2.0, 1.0
	v_lshlrev_b32_e32 v125, 16, v107
	v_mul_f32_e32 v127, 0x3d372713, v125
	v_mul_f32_e32 v127, v127, v125
	v_fma_f32 v127, v127, v125, v125
	v_mul_f32_e32 v127, 0x3f4c422a, v127
	v_add_f32_e64 v129, |v127|, |v127|
	v_mul_f32_e32 v129, 0x3fb8aa3b, v129
	v_exp_f32_e32 v129, v129
	s_nop 0
	v_add_f32_e32 v129, 1.0, v129
	v_rcp_f32_e32 v129, v129
	s_nop 0
	v_fma_f32 v129, v129, -2.0, 1.0
	v_and_b32_e32 v107, 0xffff0000, v107
	v_mul_f32_e32 v131, 0x3d372713, v107
	v_mul_f32_e32 v131, v131, v107
	v_fma_f32 v131, v131, v107, v107
	v_mul_f32_e32 v131, 0x3f4c422a, v131
	v_cmp_nlt_f32_e64 s[20:21], |v131|, s26
	s_and_saveexec_b64 s[34:35], s[20:21]
	s_xor_b64 s[20:21], exec, s[34:35]
	s_cbranch_execz .LBB0_1052
	v_add_f32_e64 v132, |v131|, |v131|
	v_mul_f32_e32 v135, 0x3fb8aa3b, v132
	v_rndne_f32_e32 v138, v135
	v_sub_f32_e32 v139, v135, v138
	v_fma_f32 v135, v132, s27, -v135
	v_fmac_f32_e32 v135, 0x32a5705f, v132
	v_add_f32_e32 v135, v139, v135
	v_cvt_i32_f32_e32 v138, v138
	v_exp_f32_e32 v135, v135
	v_cmp_ngt_f32_e32 vcc, s28, v132
	v_ldexp_f32 v135, v135, v138
	s_nop 0
	v_cndmask_b32_e32 v135, 0, v135, vcc
	v_cmp_nlt_f32_e32 vcc, s29, v132
	s_nop 1
	v_cndmask_b32_e32 v132, v158, v135, vcc
	v_add_f32_e32 v132, 1.0, v132
	v_rcp_f32_e32 v132, v132
	s_nop 0
	v_fma_f32 v138, v132, -2.0, 1.0
.LBB0_1052:
	s_andn2_saveexec_b64 s[20:21], s[20:21]
	v_mul_f32_e32 v132, v131, v131
	v_fmamk_f32 v135, v132, 0xbbbac73d, v156
	v_fmaak_f32 v135, v132, v135, 0xbd5c1c4e
	v_fmaak_f32 v135, v132, v135, 0x3e088382
	v_fmaak_f32 v135, v132, v135, 0xbeaaaa99
	v_mul_f32_e64 v135, |v131|, v135
	v_fma_f32 v138, v132, v135, |v131|
	s_or_b64 exec, exec, s[20:21]
	v_bfi_b32 v127, s30, v129, v127
	v_mul_f32_e32 v125, 0.5, v125
	v_add_f32_e32 v127, 1.0, v127
	v_mul_f32_e32 v125, v125, v127
	v_add_f32_e32 v104, v104, v134
	v_mul_f32_e32 v125, v104, v125
	v_mul_f32_e32 v104, 0.5, v108
	v_bfi_b32 v108, s30, v112, v109
	v_add_f32_e32 v108, 1.0, v108
	v_mul_f32_e32 v104, v104, v108
	v_add_f32_e32 v102, v102, v134
	v_bfi_b32 v135, s30, v123, v113
	v_mov_b32_e32 v132, v103
	v_mul_f32_e32 v104, v102, v104
	v_mul_f32_e32 v106, 0.5, v106
	v_pk_add_f32 v[102:103], v[132:133], v[134:135]
	v_bfi_b32 v135, s30, v138, v131
	v_mul_f32_e32 v103, v106, v103
	v_mul_f32_e32 v102, v102, v103
	v_mov_b32_e32 v132, v105
	v_cvt_pk_bf16_f32 v102, v104, v102
	v_mul_f32_e32 v103, 0.5, v107
	v_pk_add_f32 v[104:105], v[132:133], v[134:135]
	s_nop 0
	v_mul_f32_e32 v103, v103, v105
	v_mul_f32_e32 v103, v104, v103
	v_cvt_pk_bf16_f32 v103, v125, v103
	global_store_dwordx2 v[110:111], v[102:103], off offset:2112
	global_load_dwordx2 v[102:103], v[136:137], off offset:96
	s_waitcnt vmcnt(0)
	v_lshlrev_b32_e32 v104, 16, v102
	v_mul_f32_e32 v105, 0x3d372713, v104
	v_mul_f32_e32 v105, v105, v104
	v_fma_f32 v105, v105, v104, v104
	v_mul_f32_e32 v105, 0x3f4c422a, v105
	v_add_f32_e64 v106, |v105|, |v105|
	v_mul_f32_e32 v106, 0x3fb8aa3b, v106
	v_exp_f32_e32 v106, v106
	s_nop 0
	v_add_f32_e32 v106, 1.0, v106
	v_rcp_f32_e32 v106, v106
	s_nop 0
	v_fma_f32 v106, v106, -2.0, 1.0
	v_and_b32_e32 v102, 0xffff0000, v102
	v_mul_f32_e32 v107, 0x3d372713, v102
	v_mul_f32_e32 v107, v107, v102
	v_fma_f32 v107, v107, v102, v102
	v_mul_f32_e32 v107, 0x3f4c422a, v107
	v_add_f32_e64 v108, |v107|, |v107|
	v_mul_f32_e32 v108, 0x3fb8aa3b, v108
	v_exp_f32_e32 v108, v108
	s_nop 0
	v_add_f32_e32 v108, 1.0, v108
	v_rcp_f32_e32 v108, v108
	s_nop 0
	v_fma_f32 v108, v108, -2.0, 1.0
	v_lshlrev_b32_e32 v109, 16, v103
	v_mul_f32_e32 v112, 0x3d372713, v109
	v_mul_f32_e32 v112, v112, v109
	v_fma_f32 v112, v112, v109, v109
	v_mul_f32_e32 v112, 0x3f4c422a, v112
	v_add_f32_e64 v113, |v112|, |v112|
	v_mul_f32_e32 v113, 0x3fb8aa3b, v113
	v_exp_f32_e32 v113, v113
	s_nop 0
	v_add_f32_e32 v113, 1.0, v113
	v_rcp_f32_e32 v113, v113
	s_nop 0
	v_fma_f32 v113, v113, -2.0, 1.0
	v_and_b32_e32 v103, 0xffff0000, v103
	v_mul_f32_e32 v123, 0x3d372713, v103
	v_mul_f32_e32 v123, v123, v103
	v_fma_f32 v123, v123, v103, v103
	v_mul_f32_e32 v123, 0x3f4c422a, v123
	v_add_f32_e64 v125, |v123|, |v123|
	v_mul_f32_e32 v125, 0x3fb8aa3b, v125
	v_exp_f32_e32 v125, v125
	s_nop 0
	v_add_f32_e32 v125, 1.0, v125
	v_rcp_f32_e32 v125, v125
	s_nop 0
	v_fma_f32 v125, v125, -2.0, 1.0
	v_bfi_b32 v112, s30, v113, v112
	v_mul_f32_e32 v109, 0.5, v109
	v_add_f32_e32 v112, 1.0, v112
	v_mul_f32_e32 v109, v109, v112
	v_add_f32_e32 v100, v100, v134
	v_mul_f32_e32 v109, v100, v109
	v_mul_f32_e32 v100, 0.5, v104
	v_bfi_b32 v104, s30, v106, v105
	v_add_f32_e32 v104, 1.0, v104
	v_mul_f32_e32 v100, v100, v104
	v_add_f32_e32 v98, v98, v134
	v_bfi_b32 v135, s30, v108, v107
	v_mov_b32_e32 v132, v99
	v_mul_f32_e32 v100, v98, v100
	v_mul_f32_e32 v102, 0.5, v102
	v_pk_add_f32 v[98:99], v[132:133], v[134:135]
	v_bfi_b32 v135, s30, v125, v123
	v_mul_f32_e32 v99, v102, v99
	v_mul_f32_e32 v98, v98, v99
	v_mov_b32_e32 v132, v101
	v_cvt_pk_bf16_f32 v98, v100, v98
	v_mul_f32_e32 v99, 0.5, v103
	v_pk_add_f32 v[100:101], v[132:133], v[134:135]
	s_ashr_i32 s17, s16, 31
	v_mul_f32_e32 v99, v99, v101
	v_mul_f32_e32 v99, v100, v99
	v_cvt_pk_bf16_f32 v99, v109, v99
	v_or_b32_e32 v102, s14, v118
	v_mov_b64_e32 v[100:101], s[0:1]
	global_store_dwordx2 v[110:111], v[98:99], off offset:2144
	v_lshl_add_u64 v[98:99], s[16:17], 0, v[116:117]
	v_mad_u64_u32 v[100:101], s[16:17], v102, s25, v[100:101]
	v_mad_i32_i24 v101, s15, v157, v101
	v_lshl_add_u64 v[100:101], s[18:19], 1, v[100:101]
	v_lshl_add_u64 v[100:101], v[100:101], 0, v[114:115]
	v_add_co_u32_e32 v104, vcc, 0x1000, v100
	v_lshl_add_u64 v[98:99], v[98:99], 2, s[4:5]
	s_nop 0
	v_addc_co_u32_e32 v105, vcc, 0, v101, vcc
	global_load_dwordx2 v[104:105], v[104:105], off offset:3968
	v_mov_b32_e32 v103, s15
	global_load_dword v98, v[98:99], off offset:64
	s_waitcnt vmcnt(1)
	v_lshlrev_b32_e32 v99, 16, v104
	v_mul_f32_e32 v106, 0x3d372713, v99
	v_mul_f32_e32 v106, v106, v99
	v_fma_f32 v106, v106, v99, v99
	v_mul_f32_e32 v106, 0x3f4c422a, v106
	v_add_f32_e64 v107, |v106|, |v106|
	v_mul_f32_e32 v107, 0x3fb8aa3b, v107
	v_exp_f32_e32 v107, v107
	s_nop 0
	v_add_f32_e32 v107, 1.0, v107
	v_rcp_f32_e32 v107, v107
	s_nop 0
	v_fma_f32 v107, v107, -2.0, 1.0
	v_and_b32_e32 v104, 0xffff0000, v104
	v_mul_f32_e32 v108, 0x3d372713, v104
	v_mul_f32_e32 v108, v108, v104
	v_fma_f32 v108, v108, v104, v104
	v_mul_f32_e32 v108, 0x3f4c422a, v108
	v_add_f32_e64 v109, |v108|, |v108|
	v_mul_f32_e32 v109, 0x3fb8aa3b, v109
	v_exp_f32_e32 v109, v109
	s_nop 0
	v_add_f32_e32 v109, 1.0, v109
	v_rcp_f32_e32 v109, v109
	s_nop 0
	v_fma_f32 v109, v109, -2.0, 1.0
	v_lshlrev_b32_e32 v110, 16, v105
	v_mul_f32_e32 v111, 0x3d372713, v110
	v_mul_f32_e32 v111, v111, v110
	v_fma_f32 v111, v111, v110, v110
	v_mul_f32_e32 v111, 0x3f4c422a, v111
	v_add_f32_e64 v112, |v111|, |v111|
	v_mul_f32_e32 v112, 0x3fb8aa3b, v112
	v_exp_f32_e32 v112, v112
	s_nop 0
	v_add_f32_e32 v112, 1.0, v112
	v_rcp_f32_e32 v112, v112
	s_nop 0
	v_fma_f32 v112, v112, -2.0, 1.0
	v_and_b32_e32 v105, 0xffff0000, v105
	v_mul_f32_e32 v113, 0x3d372713, v105
	v_mul_f32_e32 v113, v113, v105
	v_fma_f32 v113, v113, v105, v105
	v_mul_f32_e32 v113, 0x3f4c422a, v113
	v_add_f32_e64 v123, |v113|, |v113|
	v_mul_f32_e32 v123, 0x3fb8aa3b, v123
	v_exp_f32_e32 v123, v123
	s_nop 0
	v_add_f32_e32 v123, 1.0, v123
	v_rcp_f32_e32 v123, v123
	s_nop 0
	v_fma_f32 v123, v123, -2.0, 1.0
	v_bfi_b32 v111, s30, v112, v111
	v_mul_f32_e32 v110, 0.5, v110
	v_add_f32_e32 v111, 1.0, v111
	v_mul_f32_e32 v110, v110, v111
	s_waitcnt vmcnt(0)
	v_add_f32_e32 v96, v96, v98
	v_mul_f32_e32 v110, v96, v110
	v_mul_f32_e32 v96, 0.5, v99
	v_bfi_b32 v99, s30, v107, v106
	v_add_f32_e32 v99, 1.0, v99
	v_mul_f32_e32 v96, v96, v99
	v_add_f32_e32 v94, v94, v98
	v_bfi_b32 v99, s30, v109, v108
	v_mov_b32_e32 v132, v95
	v_mul_f32_e32 v96, v94, v96
	v_mul_f32_e32 v104, 0.5, v104
	v_pk_add_f32 v[94:95], v[132:133], v[98:99]
	v_bfi_b32 v99, s30, v123, v113
	v_mul_f32_e32 v95, v104, v95
	v_mul_f32_e32 v94, v94, v95
	v_mov_b32_e32 v132, v97
	v_cvt_pk_bf16_f32 v96, v96, v94
	v_lshlrev_b64 v[94:95], 12, v[102:103]
	v_mul_f32_e32 v104, 0.5, v105
	v_pk_add_f32 v[102:103], v[132:133], v[98:99]
	v_lshl_add_u64 v[94:95], s[8:9], 0, v[94:95]
	v_mul_f32_e32 v97, v104, v103
	v_lshl_add_u64 v[94:95], s[18:19], 1, v[94:95]
	v_mul_f32_e32 v97, v102, v97
	v_lshl_add_u64 v[100:101], v[100:101], 0, s[10:11]
	v_lshl_add_u64 v[94:95], v[94:95], 0, v[114:115]
	v_cvt_pk_bf16_f32 v97, v110, v97
	global_store_dwordx2 v[94:95], v[96:97], off offset:2048
	global_load_dwordx2 v[96:97], v[100:101], off offset:32
	s_waitcnt vmcnt(0)
	v_lshlrev_b32_e32 v99, 16, v96
	v_mul_f32_e32 v102, 0x3d372713, v99
	v_mul_f32_e32 v102, v102, v99
	v_fma_f32 v102, v102, v99, v99
	v_mul_f32_e32 v102, 0x3f4c422a, v102
	v_add_f32_e64 v103, |v102|, |v102|
	v_mul_f32_e32 v103, 0x3fb8aa3b, v103
	v_exp_f32_e32 v103, v103
	s_nop 0
	v_add_f32_e32 v103, 1.0, v103
	v_rcp_f32_e32 v103, v103
	s_nop 0
	v_fma_f32 v103, v103, -2.0, 1.0
	v_and_b32_e32 v96, 0xffff0000, v96
	v_mul_f32_e32 v104, 0x3d372713, v96
	v_mul_f32_e32 v104, v104, v96
	v_fma_f32 v104, v104, v96, v96
	v_mul_f32_e32 v104, 0x3f4c422a, v104
	v_add_f32_e64 v105, |v104|, |v104|
	v_mul_f32_e32 v105, 0x3fb8aa3b, v105
	v_exp_f32_e32 v105, v105
	s_nop 0
	v_add_f32_e32 v105, 1.0, v105
	v_rcp_f32_e32 v105, v105
	s_nop 0
	v_fma_f32 v105, v105, -2.0, 1.0
	v_lshlrev_b32_e32 v106, 16, v97
	v_mul_f32_e32 v107, 0x3d372713, v106
	v_mul_f32_e32 v107, v107, v106
	v_fma_f32 v107, v107, v106, v106
	v_mul_f32_e32 v107, 0x3f4c422a, v107
	v_add_f32_e64 v108, |v107|, |v107|
	v_mul_f32_e32 v108, 0x3fb8aa3b, v108
	v_exp_f32_e32 v108, v108
	s_nop 0
	v_add_f32_e32 v108, 1.0, v108
	v_rcp_f32_e32 v108, v108
	s_nop 0
	v_fma_f32 v108, v108, -2.0, 1.0
	v_and_b32_e32 v97, 0xffff0000, v97
	v_mul_f32_e32 v109, 0x3d372713, v97
	v_mul_f32_e32 v109, v109, v97
	v_fma_f32 v109, v109, v97, v97
	v_mul_f32_e32 v109, 0x3f4c422a, v109
	v_add_f32_e64 v110, |v109|, |v109|
	v_mul_f32_e32 v110, 0x3fb8aa3b, v110
	v_exp_f32_e32 v110, v110
	s_nop 0
	v_add_f32_e32 v110, 1.0, v110
	v_rcp_f32_e32 v110, v110
	s_nop 0
	v_fma_f32 v110, v110, -2.0, 1.0
	v_bfi_b32 v107, s30, v108, v107
	v_mul_f32_e32 v106, 0.5, v106
	v_add_f32_e32 v107, 1.0, v107
	v_mul_f32_e32 v106, v106, v107
	v_add_f32_e32 v92, v92, v98
	v_mul_f32_e32 v106, v92, v106
	v_mul_f32_e32 v92, 0.5, v99
	v_bfi_b32 v99, s30, v103, v102
	v_add_f32_e32 v99, 1.0, v99
	v_mul_f32_e32 v92, v92, v99
	v_add_f32_e32 v90, v90, v98
	v_bfi_b32 v99, s30, v105, v104
	v_mov_b32_e32 v132, v91
	v_mul_f32_e32 v92, v90, v92
	v_mul_f32_e32 v96, 0.5, v96
	v_pk_add_f32 v[90:91], v[132:133], v[98:99]
	v_bfi_b32 v99, s30, v110, v109
	v_mul_f32_e32 v91, v96, v91
	v_mul_f32_e32 v90, v90, v91
	v_mov_b32_e32 v132, v93
	v_cvt_pk_bf16_f32 v90, v92, v90
	v_mul_f32_e32 v91, 0.5, v97
	v_pk_add_f32 v[92:93], v[132:133], v[98:99]
	s_nop 0
	v_mul_f32_e32 v91, v91, v93
	v_mul_f32_e32 v91, v92, v91
	v_cvt_pk_bf16_f32 v91, v106, v91
	global_store_dwordx2 v[94:95], v[90:91], off offset:2080
	global_load_dwordx2 v[90:91], v[100:101], off offset:64
	s_waitcnt vmcnt(0)
	v_lshlrev_b32_e32 v92, 16, v90
	v_mul_f32_e32 v93, 0x3d372713, v92
	v_mul_f32_e32 v93, v93, v92
	v_fma_f32 v93, v93, v92, v92
	v_mul_f32_e32 v93, 0x3f4c422a, v93
	v_add_f32_e64 v96, |v93|, |v93|
	v_mul_f32_e32 v96, 0x3fb8aa3b, v96
	v_exp_f32_e32 v96, v96
	s_nop 0
	v_add_f32_e32 v96, 1.0, v96
	v_rcp_f32_e32 v96, v96
	s_nop 0
	v_fma_f32 v96, v96, -2.0, 1.0
	v_and_b32_e32 v90, 0xffff0000, v90
	v_mul_f32_e32 v97, 0x3d372713, v90
	v_mul_f32_e32 v97, v97, v90
	v_fma_f32 v97, v97, v90, v90
	v_mul_f32_e32 v97, 0x3f4c422a, v97
	v_add_f32_e64 v99, |v97|, |v97|
	v_mul_f32_e32 v99, 0x3fb8aa3b, v99
	v_exp_f32_e32 v99, v99
	s_nop 0
	v_add_f32_e32 v99, 1.0, v99
	v_rcp_f32_e32 v99, v99
	s_nop 0
	v_fma_f32 v99, v99, -2.0, 1.0
	v_lshlrev_b32_e32 v102, 16, v91
	v_mul_f32_e32 v103, 0x3d372713, v102
	v_mul_f32_e32 v103, v103, v102
	v_fma_f32 v103, v103, v102, v102
	v_mul_f32_e32 v103, 0x3f4c422a, v103
	v_add_f32_e64 v104, |v103|, |v103|
	v_mul_f32_e32 v104, 0x3fb8aa3b, v104
	v_exp_f32_e32 v104, v104
	s_nop 0
	v_add_f32_e32 v104, 1.0, v104
	v_rcp_f32_e32 v104, v104
	s_nop 0
	v_fma_f32 v104, v104, -2.0, 1.0
	v_and_b32_e32 v91, 0xffff0000, v91
	v_mul_f32_e32 v105, 0x3d372713, v91
	v_mul_f32_e32 v105, v105, v91
	v_fma_f32 v105, v105, v91, v91
	v_mul_f32_e32 v105, 0x3f4c422a, v105
	v_add_f32_e64 v106, |v105|, |v105|
	v_mul_f32_e32 v106, 0x3fb8aa3b, v106
	v_exp_f32_e32 v106, v106
	s_nop 0
	v_add_f32_e32 v106, 1.0, v106
	v_rcp_f32_e32 v106, v106
	s_nop 0
	v_fma_f32 v106, v106, -2.0, 1.0
	v_bfi_b32 v103, s30, v104, v103
	v_mul_f32_e32 v102, 0.5, v102
	v_add_f32_e32 v103, 1.0, v103
	v_mul_f32_e32 v102, v102, v103
	v_add_f32_e32 v88, v88, v98
	v_mul_f32_e32 v102, v88, v102
	v_mul_f32_e32 v88, 0.5, v92
	v_bfi_b32 v92, s30, v96, v93
	v_add_f32_e32 v92, 1.0, v92
	v_mul_f32_e32 v88, v88, v92
	v_add_f32_e32 v86, v86, v98
	v_bfi_b32 v99, s30, v99, v97
	v_mov_b32_e32 v132, v87
	v_mul_f32_e32 v88, v86, v88
	v_mul_f32_e32 v90, 0.5, v90
	v_pk_add_f32 v[86:87], v[132:133], v[98:99]
	v_bfi_b32 v99, s30, v106, v105
	v_mul_f32_e32 v87, v90, v87
	v_mul_f32_e32 v86, v86, v87
	v_mov_b32_e32 v132, v89
	v_cvt_pk_bf16_f32 v86, v88, v86
	v_mul_f32_e32 v87, 0.5, v91
	v_pk_add_f32 v[88:89], v[132:133], v[98:99]
	s_nop 0
	v_mul_f32_e32 v87, v87, v89
	v_mul_f32_e32 v87, v88, v87
	v_cvt_pk_bf16_f32 v87, v102, v87
	global_store_dwordx2 v[94:95], v[86:87], off offset:2112
	global_load_dwordx2 v[86:87], v[100:101], off offset:96
	s_waitcnt vmcnt(0)
	v_lshlrev_b32_e32 v88, 16, v86
	v_mul_f32_e32 v89, 0x3d372713, v88
	v_mul_f32_e32 v89, v89, v88
	v_fma_f32 v89, v89, v88, v88
	v_mul_f32_e32 v89, 0x3f4c422a, v89
	v_add_f32_e64 v90, |v89|, |v89|
	v_mul_f32_e32 v90, 0x3fb8aa3b, v90
	v_exp_f32_e32 v90, v90
	s_nop 0
	v_add_f32_e32 v90, 1.0, v90
	v_rcp_f32_e32 v90, v90
	s_nop 0
	v_fma_f32 v90, v90, -2.0, 1.0
	v_and_b32_e32 v86, 0xffff0000, v86
	v_mul_f32_e32 v91, 0x3d372713, v86
	v_mul_f32_e32 v91, v91, v86
	v_fma_f32 v91, v91, v86, v86
	v_mul_f32_e32 v91, 0x3f4c422a, v91
	v_add_f32_e64 v92, |v91|, |v91|
	v_mul_f32_e32 v92, 0x3fb8aa3b, v92
	v_exp_f32_e32 v92, v92
	s_nop 0
	v_add_f32_e32 v92, 1.0, v92
	v_rcp_f32_e32 v92, v92
	s_nop 0
	v_fma_f32 v92, v92, -2.0, 1.0
	v_lshlrev_b32_e32 v93, 16, v87
	v_mul_f32_e32 v96, 0x3d372713, v93
	v_mul_f32_e32 v96, v96, v93
	v_fma_f32 v96, v96, v93, v93
	v_mul_f32_e32 v96, 0x3f4c422a, v96
	v_add_f32_e64 v97, |v96|, |v96|
	v_mul_f32_e32 v97, 0x3fb8aa3b, v97
	v_exp_f32_e32 v97, v97
	s_nop 0
	v_add_f32_e32 v97, 1.0, v97
	v_rcp_f32_e32 v97, v97
	s_nop 0
	v_fma_f32 v97, v97, -2.0, 1.0
	v_and_b32_e32 v87, 0xffff0000, v87
	v_mul_f32_e32 v99, 0x3d372713, v87
	v_mul_f32_e32 v99, v99, v87
	v_fma_f32 v99, v99, v87, v87
	v_mul_f32_e32 v100, 0x3f4c422a, v99
	v_cmp_nlt_f32_e64 s[14:15], |v100|, s26
	s_and_saveexec_b64 s[16:17], s[14:15]
	s_xor_b64 s[14:15], exec, s[16:17]
	s_cbranch_execz .LBB0_1132
	v_add_f32_e64 v99, |v100|, |v100|
	v_mul_f32_e32 v101, 0x3fb8aa3b, v99
	v_rndne_f32_e32 v102, v101
	v_sub_f32_e32 v103, v101, v102
	v_fma_f32 v101, v99, s27, -v101
	v_fmac_f32_e32 v101, 0x32a5705f, v99
	v_add_f32_e32 v101, v103, v101
	v_cvt_i32_f32_e32 v102, v102
	v_exp_f32_e32 v101, v101
	v_cmp_ngt_f32_e32 vcc, s28, v99
	v_ldexp_f32 v101, v101, v102
	s_nop 0
	v_cndmask_b32_e32 v101, 0, v101, vcc
	v_cmp_nlt_f32_e32 vcc, s29, v99
	s_nop 1
	v_cndmask_b32_e32 v99, v158, v101, vcc
	v_add_f32_e32 v99, 1.0, v99
	v_rcp_f32_e32 v99, v99
	s_nop 0
	v_fma_f32 v101, v99, -2.0, 1.0

.LBB0_3112:
	s_waitcnt vmcnt(0)
	v_lshlrev_b32_e32 v26, 16, v14
	v_mul_f32_e32 v27, 0x3d372713, v26
	v_mul_f32_e32 v27, v27, v26
	v_fma_f32 v27, v27, v26, v26
	v_mul_f32_e32 v27, 0x3f4c422a, v27
	v_add_f32_e64 v28, |v27|, |v27|
	v_mul_f32_e32 v28, 0x3fb8aa3b, v28
	v_exp_f32_e32 v28, v28
	s_nop 0
	v_add_f32_e32 v28, 1.0, v28
	v_rcp_f32_e32 v28, v28
	s_nop 0
	v_fma_f32 v28, v28, -2.0, 1.0
	v_and_b32_e32 v14, 0xffff0000, v14
	v_mul_f32_e32 v29, 0x3d372713, v14
	v_mul_f32_e32 v29, v29, v14
	v_fma_f32 v29, v29, v14, v14
	v_mul_f32_e32 v29, 0x3f4c422a, v29
	v_add_f32_e64 v30, |v29|, |v29|
	v_mul_f32_e32 v30, 0x3fb8aa3b, v30
	v_exp_f32_e32 v30, v30
	s_nop 0
	v_add_f32_e32 v30, 1.0, v30
	v_rcp_f32_e32 v30, v30
	s_nop 0
	v_fma_f32 v30, v30, -2.0, 1.0
	v_lshlrev_b32_e32 v31, 16, v15
	v_mul_f32_e32 v32, 0x3d372713, v31
	v_mul_f32_e32 v32, v32, v31
	v_fma_f32 v32, v32, v31, v31
	v_mul_f32_e32 v32, 0x3f4c422a, v32
	v_add_f32_e64 v33, |v32|, |v32|
	v_mul_f32_e32 v33, 0x3fb8aa3b, v33
	v_exp_f32_e32 v33, v33
	s_nop 0
	v_add_f32_e32 v33, 1.0, v33
	v_rcp_f32_e32 v33, v33
	s_nop 0
	v_fma_f32 v33, v33, -2.0, 1.0
	v_and_b32_e32 v15, 0xffff0000, v15
	v_mul_f32_e32 v34, 0x3d372713, v15
	v_mul_f32_e32 v34, v34, v15
	v_fma_f32 v34, v34, v15, v15
	v_mul_f32_e32 v34, 0x3f4c422a, v34
	v_add_f32_e64 v35, |v34|, |v34|
	v_mul_f32_e32 v35, 0x3fb8aa3b, v35
	v_exp_f32_e32 v35, v35
	s_nop 0
	v_add_f32_e32 v35, 1.0, v35
	v_rcp_f32_e32 v35, v35
	s_nop 0
	v_fma_f32 v35, v35, -2.0, 1.0
	v_lshlrev_b32_e32 v36, 16, v16
	v_mul_f32_e32 v37, 0x3d372713, v36
	v_mul_f32_e32 v37, v37, v36
	v_fma_f32 v37, v37, v36, v36
	v_mul_f32_e32 v37, 0x3f4c422a, v37
	v_add_f32_e64 v38, |v37|, |v37|
	v_mul_f32_e32 v38, 0x3fb8aa3b, v38
	v_exp_f32_e32 v38, v38
	s_nop 0
	v_add_f32_e32 v38, 1.0, v38
	v_rcp_f32_e32 v38, v38
	s_nop 0
	v_fma_f32 v38, v38, -2.0, 1.0
	v_and_b32_e32 v16, 0xffff0000, v16
	v_mul_f32_e32 v39, 0x3d372713, v16
	v_mul_f32_e32 v39, v39, v16
	v_fma_f32 v39, v39, v16, v16
	v_mul_f32_e32 v39, 0x3f4c422a, v39
	v_add_f32_e64 v40, |v39|, |v39|
	v_mul_f32_e32 v40, 0x3fb8aa3b, v40
	v_exp_f32_e32 v40, v40
	s_nop 0
	v_add_f32_e32 v40, 1.0, v40
	v_rcp_f32_e32 v40, v40
	s_nop 0
	v_fma_f32 v40, v40, -2.0, 1.0
	v_lshlrev_b32_e32 v41, 16, v17
	v_mul_f32_e32 v42, 0x3d372713, v41
	v_mul_f32_e32 v42, v42, v41
	v_fma_f32 v42, v42, v41, v41
	v_mul_f32_e32 v42, 0x3f4c422a, v42
	v_add_f32_e64 v43, |v42|, |v42|
	v_mul_f32_e32 v43, 0x3fb8aa3b, v43
	v_exp_f32_e32 v43, v43
	s_nop 0
	v_add_f32_e32 v43, 1.0, v43
	v_rcp_f32_e32 v43, v43
	s_nop 0
	v_fma_f32 v43, v43, -2.0, 1.0
	v_and_b32_e32 v17, 0xffff0000, v17
	v_mul_f32_e32 v44, 0x3d372713, v17
	v_mul_f32_e32 v44, v44, v17
	v_fma_f32 v44, v44, v17, v17
	v_mul_f32_e32 v44, 0x3f4c422a, v44
	v_add_f32_e64 v45, |v44|, |v44|
	v_mul_f32_e32 v45, 0x3fb8aa3b, v45
	v_exp_f32_e32 v45, v45
	s_nop 0
	v_add_f32_e32 v45, 1.0, v45
	v_rcp_f32_e32 v45, v45
	s_nop 0
	v_fma_f32 v45, v45, -2.0, 1.0
	v_lshlrev_b32_e32 v46, 16, v10
	v_mul_f32_e32 v47, 0x3d372713, v46
	v_mul_f32_e32 v47, v47, v46
	v_fma_f32 v47, v47, v46, v46
	v_mul_f32_e32 v47, 0x3f4c422a, v47
	v_add_f32_e64 v48, |v47|, |v47|
	v_mul_f32_e32 v48, 0x3fb8aa3b, v48
	v_exp_f32_e32 v48, v48
	s_nop 0
	v_add_f32_e32 v48, 1.0, v48
	v_rcp_f32_e32 v48, v48
	s_nop 0
	v_fma_f32 v48, v48, -2.0, 1.0
	v_and_b32_e32 v10, 0xffff0000, v10
	v_mul_f32_e32 v49, 0x3d372713, v10
	v_mul_f32_e32 v49, v49, v10
	v_fma_f32 v49, v49, v10, v10
	v_mul_f32_e32 v49, 0x3f4c422a, v49
	v_cmp_nlt_f32_e64 s[0:1], |v49|, s9
	s_and_saveexec_b64 s[2:3], s[0:1]
	s_xor_b64 s[0:1], exec, s[2:3]
	s_cbranch_execz .LBB0_3150
	v_add_f32_e64 v55, |v49|, |v49|
	s_waitcnt lgkmcnt(0)
	v_mul_f32_e32 v56, 0x3fb8aa3b, v55
	v_rndne_f32_e32 v57, v56
	v_sub_f32_e32 v58, v56, v57
	v_fma_f32 v56, v55, s10, -v56
	v_fmac_f32_e32 v56, 0x32a5705f, v55
	v_add_f32_e32 v56, v58, v56
	v_cvt_i32_f32_e32 v57, v57
	v_exp_f32_e32 v56, v56
	v_cmp_ngt_f32_e32 vcc, s11, v55
	v_ldexp_f32 v56, v56, v57
	s_nop 0
	v_cndmask_b32_e32 v56, 0, v56, vcc
	v_cmp_nlt_f32_e32 vcc, s14, v55
	s_nop 1
	v_cndmask_b32_e32 v55, v54, v56, vcc
	v_add_f32_e32 v55, 1.0, v55
	v_rcp_f32_e32 v55, v55
	s_nop 0
	v_fma_f32 v55, v55, -2.0, 1.0

.LBB0_3152:
	s_or_b64 exec, exec, s[0:1]
	s_waitcnt lgkmcnt(0)
	v_lshlrev_b32_e32 v56, 16, v11
	v_mul_f32_e32 v57, 0x3d372713, v56
	v_mul_f32_e32 v57, v57, v56
	v_fma_f32 v57, v57, v56, v56
	v_mul_f32_e32 v57, 0x3f4c422a, v57
	v_add_f32_e64 v58, |v57|, |v57|
	v_mul_f32_e32 v58, 0x3fb8aa3b, v58
	v_exp_f32_e32 v58, v58
	s_nop 0
	v_add_f32_e32 v58, 1.0, v58
	v_rcp_f32_e32 v58, v58
	s_nop 0
	v_fma_f32 v58, v58, -2.0, 1.0
	v_and_b32_e32 v11, 0xffff0000, v11
	v_mul_f32_e32 v59, 0x3d372713, v11
	v_mul_f32_e32 v59, v59, v11
	v_fma_f32 v59, v59, v11, v11
	v_mul_f32_e32 v59, 0x3f4c422a, v59
	v_add_f32_e64 v60, |v59|, |v59|
	v_mul_f32_e32 v60, 0x3fb8aa3b, v60
	v_exp_f32_e32 v60, v60
	s_nop 0
	v_add_f32_e32 v60, 1.0, v60
	v_rcp_f32_e32 v60, v60
	s_nop 0
	v_fma_f32 v60, v60, -2.0, 1.0
	v_lshlrev_b32_e32 v61, 16, v12
	v_mul_f32_e32 v62, 0x3d372713, v61
	v_mul_f32_e32 v62, v62, v61
	v_fma_f32 v62, v62, v61, v61
	v_mul_f32_e32 v62, 0x3f4c422a, v62
	v_add_f32_e64 v63, |v62|, |v62|
	v_mul_f32_e32 v63, 0x3fb8aa3b, v63
	v_exp_f32_e32 v63, v63
	s_nop 0
	v_add_f32_e32 v63, 1.0, v63
	v_rcp_f32_e32 v63, v63
	s_nop 0
	v_fma_f32 v63, v63, -2.0, 1.0
	v_and_b32_e32 v12, 0xffff0000, v12
	v_mul_f32_e32 v64, 0x3d372713, v12
	v_mul_f32_e32 v64, v64, v12
	v_fma_f32 v64, v64, v12, v12
	v_mul_f32_e32 v64, 0x3f4c422a, v64
	v_add_f32_e64 v65, |v64|, |v64|
	v_mul_f32_e32 v65, 0x3fb8aa3b, v65
	v_exp_f32_e32 v65, v65
	s_nop 0
	v_add_f32_e32 v65, 1.0, v65
	v_rcp_f32_e32 v65, v65
	s_nop 0
	v_fma_f32 v65, v65, -2.0, 1.0
	v_lshlrev_b32_e32 v66, 16, v13
	v_mul_f32_e32 v67, 0x3d372713, v66
	v_mul_f32_e32 v67, v67, v66
	v_fma_f32 v67, v67, v66, v66
	v_mul_f32_e32 v67, 0x3f4c422a, v67
	v_add_f32_e64 v68, |v67|, |v67|
	v_mul_f32_e32 v68, 0x3fb8aa3b, v68
	v_exp_f32_e32 v68, v68
	s_nop 0
	v_add_f32_e32 v68, 1.0, v68
	v_rcp_f32_e32 v68, v68
	s_nop 0
	v_fma_f32 v68, v68, -2.0, 1.0
	v_and_b32_e32 v13, 0xffff0000, v13
	v_mul_f32_e32 v69, 0x3d372713, v13
	v_mul_f32_e32 v69, v69, v13
	v_fma_f32 v69, v69, v13, v13
	v_mul_f32_e32 v69, 0x3f4c422a, v69
	v_add_f32_e64 v70, |v69|, |v69|
	v_mul_f32_e32 v70, 0x3fb8aa3b, v70
	v_exp_f32_e32 v70, v70
	s_nop 0
	v_add_f32_e32 v70, 1.0, v70
	v_rcp_f32_e32 v70, v70
	s_nop 0
	v_fma_f32 v70, v70, -2.0, 1.0
	v_lshlrev_b32_e32 v71, 16, v6
	v_mul_f32_e32 v72, 0x3d372713, v71
	v_mul_f32_e32 v72, v72, v71
	v_fma_f32 v72, v72, v71, v71
	v_mul_f32_e32 v72, 0x3f4c422a, v72
	v_add_f32_e64 v73, |v72|, |v72|
	v_mul_f32_e32 v73, 0x3fb8aa3b, v73
	v_exp_f32_e32 v73, v73
	s_nop 0
	v_add_f32_e32 v73, 1.0, v73
	v_rcp_f32_e32 v73, v73
	s_nop 0
	v_fma_f32 v73, v73, -2.0, 1.0
	v_and_b32_e32 v74, 0xffff0000, v6
	v_mul_f32_e32 v6, 0x3d372713, v74
	v_mul_f32_e32 v6, v6, v74
	v_fma_f32 v6, v6, v74, v74
	v_mul_f32_e32 v75, 0x3f4c422a, v6
	v_cmp_nlt_f32_e64 s[0:1], |v75|, s9
	s_and_saveexec_b64 s[2:3], s[0:1]
	s_xor_b64 s[0:1], exec, s[2:3]
	s_cbranch_execz .LBB0_3182
	v_add_f32_e64 v6, |v75|, |v75|
	v_mul_f32_e32 v76, 0x3fb8aa3b, v6
	v_rndne_f32_e32 v77, v76
	v_sub_f32_e32 v78, v76, v77
	v_fma_f32 v76, v6, s10, -v76
	v_fmac_f32_e32 v76, 0x32a5705f, v6
	v_add_f32_e32 v76, v78, v76
	v_cvt_i32_f32_e32 v77, v77
	v_exp_f32_e32 v76, v76
	v_cmp_ngt_f32_e32 vcc, s11, v6
	v_ldexp_f32 v76, v76, v77
	s_nop 0
	v_cndmask_b32_e32 v76, 0, v76, vcc
	v_cmp_nlt_f32_e32 vcc, s14, v6
	s_nop 1
	v_cndmask_b32_e32 v6, v54, v76, vcc
	v_add_f32_e32 v6, 1.0, v6
	v_rcp_f32_e32 v6, v6
	s_nop 0
	v_fma_f32 v76, v6, -2.0, 1.0

.LBB0_3206:
	s_andn2_saveexec_b64 s[0:1], s[0:1]
	v_mul_f32_e32 v6, v91, v91
	v_fmamk_f32 v7, v6, 0xbbbac73d, v51
	v_fmaak_f32 v7, v6, v7, 0xbd5c1c4e
	v_fmaak_f32 v7, v6, v7, 0x3e088382
	v_fmaak_f32 v7, v6, v7, 0xbeaaaa99
	v_mul_f32_e64 v7, |v91|, v7
	v_fma_f32 v92, v6, v7, |v91|
	s_or_b64 exec, exec, s[0:1]
	v_lshlrev_b32_e32 v6, 16, v2
	v_mul_f32_e32 v7, 0x3d372713, v6
	v_mul_f32_e32 v7, v7, v6
	v_fma_f32 v7, v7, v6, v6
	v_mul_f32_e32 v7, 0x3f4c422a, v7
	v_add_f32_e64 v93, |v7|, |v7|
	v_mul_f32_e32 v93, 0x3fb8aa3b, v93
	v_exp_f32_e32 v93, v93
	s_nop 0
	v_add_f32_e32 v93, 1.0, v93
	v_rcp_f32_e32 v93, v93
	s_nop 0
	v_fma_f32 v93, v93, -2.0, 1.0
	v_and_b32_e32 v94, 0xffff0000, v2
	v_mul_f32_e32 v2, 0x3d372713, v94
	v_mul_f32_e32 v2, v2, v94
	v_fma_f32 v2, v2, v94, v94
	v_mul_f32_e32 v95, 0x3f4c422a, v2
	v_cmp_nlt_f32_e64 s[0:1], |v95|, s9
	s_and_saveexec_b64 s[2:3], s[0:1]
	s_xor_b64 s[0:1], exec, s[2:3]
	s_cbranch_execz .LBB0_3214
	v_add_f32_e64 v2, |v95|, |v95|
	v_mul_f32_e32 v96, 0x3fb8aa3b, v2
	v_rndne_f32_e32 v97, v96
	v_sub_f32_e32 v98, v96, v97
	v_fma_f32 v96, v2, s10, -v96
	v_fmac_f32_e32 v96, 0x32a5705f, v2
	v_add_f32_e32 v96, v98, v96
	v_cvt_i32_f32_e32 v97, v97
	v_exp_f32_e32 v96, v96
	v_cmp_ngt_f32_e32 vcc, s11, v2
	v_ldexp_f32 v96, v96, v97
	s_nop 0
	v_cndmask_b32_e32 v96, 0, v96, vcc
	v_cmp_nlt_f32_e32 vcc, s14, v2
	s_nop 1
	v_cndmask_b32_e32 v2, v54, v96, vcc
	v_add_f32_e32 v2, 1.0, v2
	v_rcp_f32_e32 v2, v2
	s_nop 0
	v_fma_f32 v96, v2, -2.0, 1.0
